# w_dn conversion tiles hosted in attention KV loop (quarters) and MoE-1 epilogues; mLSTM phase converts w_gu only
# speedup vs baseline: 1.0136x; 1.0094x over previous
; #define LAS __attribute__((address_space(3)))
; __global__ void __launch_bounds__(NTHREADS, 2) fwd(Args args) {
;     extern __shared__ __attribute__((aligned(16))) unsigned char lds_raw[];
;     LAS unsigned char* lds = (LAS unsigned char*)lds_raw;
;     volatile LAS unsigned* MISC = (volatile LAS unsigned*)(lds + MISC_OFF);
;     const int wave = __builtin_amdgcn_readfirstlane((int)threadIdx.x >> 6);
;     const int G = gridDim.x, bx = blockIdx.x;
;     const int vcu = (G % 8 == 0) ? (bx % 8) * (G / 8) + bx / 8 : bx;
_Z3fwd4Args:
	s_load_dword s73, s[0:1], 0xc8
	s_mov_b32 s76, s2
	s_add_u32 s2, s0, 0xc8
	s_addc_u32 s3, s1, 0
	v_readfirstlane_b32 s20, v0
	v_writelane_b32 v254, s2, 0
	s_lshl_b32 s99, s76, 3
	s_lshr_b32 s98, s20, 6
	s_add_i32 s98, s98, s99
	s_add_i32 s98, s98, 0x14000
	s_mov_b32 s99, 0
	s_mov_b32 s74, s76
	s_nop 0
	v_writelane_b32 v254, s3, 1
	s_waitcnt lgkmcnt(0)
	s_and_b32 s2, s73, 7
	s_cmp_lg_u32 s2, 0
	s_cbranch_scc1 .LBB0_2
	s_ashr_i32 s3, s76, 31
	s_lshr_b32 s3, s3, 29
	s_add_i32 s3, s76, s3
	s_and_b32 s4, s3, -8
	s_ashr_i32 s2, s73, 3
	s_sub_i32 s4, s76, s4
	s_mul_i32 s2, s2, s4
	s_ashr_i32 s3, s3, 3
	s_add_i32 s74, s2, s3

; __device__ __forceinline__ int lane_id_() { int l; asm volatile("v_mbcnt_lo_u32_b32 %0, -1, 0\n\tv_mbcnt_hi_u32_b32 %0, -1, %0" : "=v"(l)); return l; }
; __global__ void __launch_bounds__(NTHREADS, 2) fwd(Args args) {
;     ...
;     if (IN(4)) {
;         const int lane = lane_id_(), tid = wave * 64 + lane; (void)tid; (void)lane;
;         const bool att_first = (vcu & 1) != 0;
;     ...
;         if (att_first) { ATT_BLOCK(); __syncthreads(); }
; #pragma unroll 1
;         for (int rep_ = 0; rep_ < NREP(4); ++rep_) {
;             ml::Conv cvs{w_gu, w_dn, WTGU, WTDN, bx * 8 + wave, G * 8};
.LBB0_504:
	s_mov_b32 s99, 0
	v_readlane_b32 s0, v254, 34
	v_readlane_b32 s14, v254, 48
	v_readlane_b32 s1, v254, 35
	v_readlane_b32 s15, v254, 49
	s_add_u32 s0, s14, 0x4d59400
	s_addc_u32 s1, s15, 0
	v_writelane_b32 v255, s0, 16
	v_readlane_b32 s2, v254, 36
	v_readlane_b32 s3, v254, 37
	v_writelane_b32 v255, s1, 17
	s_add_u32 s0, s14, 0x14d59400
	v_writelane_b32 v255, s0, 18
	s_addc_u32 s0, s15, 0
	s_add_u32 s66, s14, 0x318e9400
	s_addc_u32 s67, s15, 0
	s_add_u32 s68, s14, 0x338e9400
	s_addc_u32 s69, s15, 0
	s_add_u32 s57, s14, 0x4de49400
	v_writelane_b32 v255, s0, 19
	s_addc_u32 s0, s15, 0
	s_cmp_lt_i32 s96, 5
	v_writelane_b32 v255, s0, 20
	s_cselect_b64 s[0:1], -1, 0
	s_cmp_gt_i32 s97, 4
	s_cselect_b64 s[2:3], -1, 0
	s_and_b64 s[0:1], s[0:1], s[2:3]
	v_writelane_b32 v255, s0, 21
	s_andn2_b64 vcc, exec, s[0:1]
	v_readlane_b32 s4, v254, 38
	v_writelane_b32 v255, s1, 22
	v_writelane_b32 v255, s76, 23
	v_writelane_b32 v255, s77, 24
	v_writelane_b32 v255, s74, 25
	v_readlane_b32 s5, v254, 39
	v_readlane_b32 s6, v254, 40
	v_readlane_b32 s7, v254, 41
	v_readlane_b32 s8, v254, 42
	v_readlane_b32 s9, v254, 43
	v_readlane_b32 s10, v254, 44
	v_readlane_b32 s11, v254, 45
	v_readlane_b32 s12, v254, 46
	v_readlane_b32 s13, v254, 47
	s_cbranch_vccnz .LBB0_659
	s_bitcmp0_b32 s74, 0
	s_cselect_b64 s[0:1], -1, 0
	v_writelane_b32 v255, s0, 26
	s_and_b64 vcc, exec, s[0:1]
	v_mbcnt_lo_u32_b32 v180, -1, 0
	v_mbcnt_hi_u32_b32 v180, -1, v180
	s_nop 0
	v_writelane_b32 v255, s1, 27
	s_cbranch_vccnz .LBB0_529
.Latt1_entry:
	s_cmpk_gt_i32 s74, 0x1ff
	v_readlane_b32 s40, v255, 4
	v_readlane_b32 s41, v255, 5
	s_cbranch_scc1 .LBB0_528
	s_lshl_b32 s0, s84, 2
	s_add_i32 s29, s0, 0
	s_lshl_b32 s0, s77, 13
	s_mov_b32 s7, 0
	s_lshl_b32 s6, s77, 5
	s_add_i32 s0, s0, 0
	s_add_i32 s29, s29, 0x10000
	s_add_i32 s0, s0, 0x11000
	s_lshl_b64 s[2:3], s[6:7], 11
	s_add_u32 s1, s57, s2
	v_readlane_b32 s2, v255, 20
	v_readlane_b32 s8, v254, 34
	s_addc_u32 s33, s2, s3
	v_readlane_b32 s22, v254, 48
	v_readlane_b32 s9, v254, 35
	v_readlane_b32 s10, v254, 36
	v_readlane_b32 s11, v254, 37
	v_readlane_b32 s12, v254, 38
	v_readlane_b32 s13, v254, 39
	v_readlane_b32 s14, v254, 40
	v_readlane_b32 s15, v254, 41
	v_readlane_b32 s16, v254, 42
	v_readlane_b32 s17, v254, 43
	v_readlane_b32 s18, v254, 44
	v_readlane_b32 s19, v254, 45
	v_readlane_b32 s20, v254, 46
	v_readlane_b32 s21, v254, 47
	v_readlane_b32 s23, v254, 49
	s_add_u32 s26, s22, 0x29031400
	s_addc_u32 s27, s23, 0
	v_mov_b32_e32 v177, 0
	s_mov_b32 s52, 0x42b504f3
	s_mov_b32 s28, 0x3e0293ee
	v_mov_b32_e32 v181, 0xf149f2ca
	s_mov_b64 s[30:31], 0x20000
	v_mov_b32_e32 v182, 0x240000
	s_mov_b32 s8, s7
	s_mov_b32 s9, s7
	s_mov_b32 s10, s7
	s_mov_b32 s11, s7
	s_mov_b32 s12, s7
	s_mov_b32 s13, s7
	s_mov_b32 s14, s7
	s_mov_b32 s15, s7
	s_mov_b32 s16, s7
	s_mov_b32 s17, s7
	s_mov_b32 s18, s7
	s_mov_b32 s19, s7
	s_mov_b32 s20, s7
	s_mov_b32 s21, s7
	s_mov_b32 s22, s7
	s_mov_b32 s23, s7
	s_mov_b32 s7, 0xc3e00000
	v_mov_b32_e32 v183, 0x43e00000
	s_mov_b32 s53, s74
	s_branch .LBB0_509

; #define SBAR() __builtin_amdgcn_sched_barrier(0)
; #define SLOAD(i, k0) do { sr_[i].vs0 = *reinterpret_cast<const bf16x8*>(&Vh[(long)((k0) + sr) * LDK + sc]); sr_[i].vs1 = *reinterpret_cast<const bf16x8*>(&Vh[(long)((k0) + 32 + sr) * LDK + sc]); \
;     sr_[i].ks0 = *reinterpret_cast<const bf16x8*>(&Kh[(long)((k0) + sr) * LDK + sc]); sr_[i].ks1 = *reinterpret_cast<const bf16x8*>(&Kh[(long)((k0) + 32 + sr) * LDK + sc]); } while (0)
; __device__ __forceinline__ void attn_dense_body(const bf16_t* __restrict__ Qb, const bf16_t* __restrict__ Kh, const bf16_t* __restrict__ Vh,
;                                                 unsigned char* __restrict__ Ob, int seq, char* lds, LAS unsigned char* lds3, const int wave_) {
;     ...
;     SBAR(); qkt(pB0, pB1, (bf16_t*)((char*)K_lds + SHM_K), qr, r32, hi);
;     finishSM(pA0, pA1, alA, l_reg, pa0, pa1, pa2, pa3); SBAR();
;     SLOAD(SO, (j + 2) * KVBLK); SBAR();
;     pv_d0(o, vb0, pa0, pa1, pa2, pa3); partialSM(pB0, pB1, m_reg, mnB, alB);
.LBB0_510:
	ds_read_b128 v[64:67], v200 offset:49152
	ds_read_b128 v[68:71], v200 offset:57344
	ds_read_b128 v[212:215], v202 offset:49152
	ds_read_b128 v[216:219], v202 offset:57344
	v_add_f32_e32 v160, 0, v175
	v_add_f32_e32 v160, v210, v160
	s_waitcnt lgkmcnt(3)
	v_mfma_f32_32x32x16_bf16 v[80:95], v[64:67], v[116:119], 0
	v_add_f32_e32 v160, v161, v160
	v_add_f32_e32 v160, v207, v160
	v_add_f32_e32 v160, v162, v160
	v_add_f32_e32 v160, v174, v160
	v_add_f32_e32 v160, v163, v160
	v_add_f32_e32 v160, v173, v160
	v_add_f32_e32 v160, v164, v160
	s_waitcnt lgkmcnt(2)
	v_mfma_f32_32x32x16_bf16 v[64:79], v[68:71], v[116:119], 0
	v_add_f32_e32 v160, v172, v160
	v_add_f32_e32 v160, v165, v160
	v_add_f32_e32 v160, v171, v160
	v_exp_f32_e32 v156, v156
	v_add_f32_e32 v160, v166, v160
	v_exp_f32_e32 v157, v157
	v_add_f32_e32 v160, v170, v160
	s_waitcnt lgkmcnt(1)
	v_mfma_f32_32x32x16_bf16 v[80:95], v[212:215], v[112:115], v[80:95]
	v_exp_f32_e32 v154, v154
	v_add_f32_e32 v160, v167, v160
	v_exp_f32_e32 v155, v155
	v_add_f32_e32 v160, v169, v160
	v_exp_f32_e32 v148, v148
	v_add_f32_e32 v160, v156, v160
	v_exp_f32_e32 v149, v149
	s_waitcnt lgkmcnt(0)
	v_mfma_f32_32x32x16_bf16 v[64:79], v[216:219], v[112:115], v[64:79]
	ds_read_b128 v[212:215], v201 offset:49152
	ds_read_b128 v[216:219], v201 offset:57344
	v_add_f32_e32 v160, v157, v160
	v_exp_f32_e32 v146, v146
	v_add_f32_e32 v160, v154, v160
	v_exp_f32_e32 v147, v147
	v_add_f32_e32 v160, v155, v160
	v_exp_f32_e32 v144, v144
	s_waitcnt lgkmcnt(1)
	v_mfma_f32_32x32x16_bf16 v[80:95], v[212:215], v[124:127], v[80:95]
	v_add_f32_e32 v160, v148, v160
	v_exp_f32_e32 v145, v145
	v_add_f32_e32 v160, v149, v160
	v_exp_f32_e32 v158, v158
	v_add_f32_e32 v160, v146, v160
	v_exp_f32_e32 v159, v159
	v_add_f32_e32 v160, v147, v160
	s_waitcnt lgkmcnt(0)
	v_mfma_f32_32x32x16_bf16 v[64:79], v[216:219], v[124:127], v[64:79]
	ds_read_b128 v[212:215], v198 offset:49152
	ds_read_b128 v[216:219], v198 offset:57344
	v_exp_f32_e32 v152, v152
	v_add_f32_e32 v160, v144, v160
	v_exp_f32_e32 v153, v153
	v_add_f32_e32 v160, v145, v160
	v_exp_f32_e32 v150, v150
	v_add_f32_e32 v160, v158, v160
	s_waitcnt lgkmcnt(1)
	v_mfma_f32_32x32x16_bf16 v[80:95], v[212:215], v[120:123], v[80:95]
	v_exp_f32_e32 v151, v151
	v_add_f32_e32 v160, v159, v160
	v_add_f32_e32 v160, v152, v160
	v_add_f32_e32 v160, v153, v160
	v_add_f32_e32 v160, v150, v160
	v_add_f32_e32 v204, v151, v160
	v_mov_b32_e32 v205, v204
	s_waitcnt lgkmcnt(0)
	v_mfma_f32_32x32x16_bf16 v[64:79], v[216:219], v[120:123], v[64:79]
	ds_read_b128 v[212:215], v197 offset:49152
	ds_read_b128 v[216:219], v197 offset:57344
	v_permlane32_swap_b32_e32 v204, v205
	s_waitcnt lgkmcnt(1)
	v_mfma_f32_32x32x16_bf16 v[80:95], v[212:215], v[108:111], v[80:95]
	s_waitcnt lgkmcnt(0)
	v_mfma_f32_32x32x16_bf16 v[64:79], v[216:219], v[108:111], v[64:79]
	ds_read_b128 v[212:215], v196 offset:49152
	ds_read_b128 v[216:219], v196 offset:57344
	s_waitcnt lgkmcnt(1)
	v_mfma_f32_32x32x16_bf16 v[80:95], v[212:215], v[104:107], v[80:95]
	s_waitcnt lgkmcnt(0)
	v_mfma_f32_32x32x16_bf16 v[64:79], v[216:219], v[104:107], v[64:79]
	ds_read_b128 v[212:215], v195 offset:49152
	ds_read_b128 v[216:219], v195 offset:57344
	s_waitcnt lgkmcnt(1)
	v_mfma_f32_32x32x16_bf16 v[80:95], v[212:215], v[100:103], v[80:95]
	s_waitcnt lgkmcnt(0)
	v_mfma_f32_32x32x16_bf16 v[64:79], v[216:219], v[100:103], v[64:79]
	ds_read_b128 v[212:215], v192 offset:49152
	ds_read_b128 v[216:219], v192 offset:57344
	v_cvt_pk_bf16_f32 v160, v175, v210
	v_cvt_pk_bf16_f32 v161, v161, v207
	v_cvt_pk_bf16_f32 v162, v162, v174
	v_cvt_pk_bf16_f32 v163, v163, v173
	v_cvt_pk_bf16_f32 v164, v164, v172
	v_cvt_pk_bf16_f32 v165, v165, v171
	s_waitcnt lgkmcnt(1)
	v_mfma_f32_32x32x16_bf16 v[80:95], v[212:215], v[96:99], v[80:95]
	v_cvt_pk_bf16_f32 v166, v166, v170
	v_cvt_pk_bf16_f32 v167, v167, v169
	v_cvt_pk_bf16_f32 v170, v156, v157
	v_cvt_pk_bf16_f32 v171, v154, v155
	v_cvt_pk_bf16_f32 v172, v148, v149
	v_cvt_pk_bf16_f32 v173, v146, v147
	v_cvt_pk_bf16_f32 v206, v144, v145
	s_waitcnt lgkmcnt(0)
	v_mfma_f32_32x32x16_bf16 v[64:79], v[216:219], v[96:99], v[64:79]
	v_cvt_pk_bf16_f32 v207, v158, v159
	v_cvt_pk_bf16_f32 v208, v152, v153
	v_permlane32_swap_b32_e32 v160, v162
	v_cvt_pk_bf16_f32 v209, v150, v151
	v_permlane32_swap_b32_e32 v206, v208
	v_permlane32_swap_b32_e32 v161, v163
	v_permlane32_swap_b32_e32 v164, v166
	v_permlane32_swap_b32_e32 v165, v167
	v_permlane32_swap_b32_e32 v170, v172
	v_permlane32_swap_b32_e32 v171, v173
	v_permlane32_swap_b32_e32 v207, v209
	s_mov_b32 s4, 0xff6e8000
	v_add_co_u32_e32 v144, vcc, s4, v178
	s_mov_b32 s4, 0xff6f0000
	s_nop 0
	v_addc_co_u32_e32 v145, vcc, -1, v179, vcc
	v_add_co_u32_e32 v148, vcc, s4, v178
	s_mov_b32 s4, 0xfffe8000
	s_nop 0
	v_addc_co_u32_e32 v149, vcc, -1, v179, vcc
	v_add_co_u32_e32 v152, vcc, s4, v178
	s_mov_b32 s4, 0xffff0000
	s_nop 0
	v_addc_co_u32_e32 v153, vcc, -1, v179, vcc
	v_add_co_u32_e32 v156, vcc, s4, v178
	global_load_dwordx4 v[144:147], v[144:145], off
	s_nop 0
	global_load_dwordx4 v[148:151], v[148:149], off
	v_addc_co_u32_e32 v157, vcc, -1, v179, vcc
	global_load_dwordx4 v[152:155], v[152:153], off
	s_nop 0
	global_load_dwordx4 v[156:159], v[156:157], off
	s_min_u32 s101, s99, 31
	v_mov_b32_e32 v253, s101
	v_and_b32_e32 v253, 3, v253
	s_lshr_b32 s100, s101, 2
	s_add_i32 s100, s100, 32
	s_lshl_b32 s100, s100, 11
	s_and_b32 s101, s98, 0x7ff
	s_add_i32 s100, s100, s101
	s_sub_i32 s101, s100, 0x10000
	s_lshr_b32 s101, s101, 10
	s_lshl_b32 s101, s101, 24
	v_mov_b32_e32 v252, s101
	s_bfe_u32 s101, s100, 0x40006
	s_lshl_b32 s101, s101, 20
	v_add_u32_e32 v252, s101, v252
	s_and_b32 s101, s100, 63
	s_lshl_b32 s101, s101, 7
	v_add_u32_e32 v252, s101, v252
	v_mbcnt_lo_u32_b32 v251, -1, 0
	v_mbcnt_hi_u32_b32 v251, -1, v251
	v_lshrrev_b32_e32 v250, 3, v251
	v_and_b32_e32 v251, 7, v251
	v_lshl_add_u32 v252, v250, 17, v252
	v_lshl_add_u32 v252, v251, 4, v252
	v_lshl_add_u32 v252, v253, 15, v252
	v_readlane_b32 s100, v254, 42
	v_readlane_b32 s101, v254, 43
	s_nop 4
	global_load_dwordx4 v[232:235], v252, s[100:101] nt
	v_add_u32_e32 v252, 0x2000, v252
	global_load_dwordx4 v[236:239], v252, s[100:101] nt
	v_add_u32_e32 v252, 0x2000, v252
	global_load_dwordx4 v[240:243], v252, s[100:101] nt
	v_add_u32_e32 v252, 0x2000, v252
	global_load_dwordx4 v[244:247], v252, s[100:101] nt
	ds_read_b64_tr_b16 v[210:211], v190 offset:0
	ds_read_b64_tr_b16 v[212:213], v190 offset:0x800
	ds_read_b64_tr_b16 v[214:215], v190 offset:0x1000
	ds_read_b64_tr_b16 v[216:217], v190 offset:0x1800
	ds_read_b64_tr_b16 v[218:219], v190 offset:0x2000
	ds_read_b64_tr_b16 v[220:221], v190 offset:0x2800
	ds_read_b64_tr_b16 v[222:223], v190 offset:0x3000
	ds_read_b64_tr_b16 v[224:225], v190 offset:0x3800
	s_waitcnt lgkmcnt(0)
; #define LAS __attribute__((address_space(3)))
; template <int D0> __device__ __forceinline__ void pv_one(f32x16& od, int vb, bf16x8 pa0, bf16x8 pa1, bf16x8 pa2, bf16x8 pa3) {
;   const s16x4 l0 = tr_read<v_rd_off(D0, 0, 0)>(vb), h0 = tr_read<v_rd_off(D0, 0, 1)>(vb), l1 = tr_read<v_rd_off(D0, 1, 0)>(vb), h1 = tr_read<v_rd_off(D0, 1, 1)>(vb);
;   const s16x4 l2 = tr_read<v_rd_off(D0, 2, 0)>(vb), h2 = tr_read<v_rd_off(D0, 2, 1)>(vb), l3 = tr_read<v_rd_off(D0, 3, 0)>(vb), h3 = tr_read<v_rd_off(D0, 3, 1)>(vb);
;   asm volatile("s_waitcnt lgkmcnt(0)" ::: "memory"); SBAR();
;     ...
;   od = __builtin_amdgcn_mfma_f32_32x32x16_bf16(pa0, PK(l0, h0), od, 0, 0, 0);
;   od = __builtin_amdgcn_mfma_f32_32x32x16_bf16(pa1, PK(l1, h1), od, 0, 0, 0);
;   od = __builtin_amdgcn_mfma_f32_32x32x16_bf16(pa2, PK(l2, h2), od, 0, 0, 0);
;   od = __builtin_amdgcn_mfma_f32_32x32x16_bf16(pa3, PK(l3, h3), od, 0, 0, 0);
;     ...
; }
; __device__ __forceinline__ void pv_d0(f32x16* o, int vb, bf16x8 pa0, bf16x8 pa1, bf16x8 pa2, bf16x8 pa3) {
;   pv_one<0>(o[0], vb, pa0, pa1, pa2, pa3); pv_one<1>(o[1], vb, pa0, pa1, pa2, pa3); pv_one<2>(o[2], vb, pa0, pa1, pa2, pa3); pv_one<3>(o[3], vb, pa0, pa1, pa2, pa3);
; }
; __device__ __forceinline__ void attn_dense_body(const bf16_t* __restrict__ Qb, const bf16_t* __restrict__ Kh, const bf16_t* __restrict__ Vh,
;                                                 unsigned char* __restrict__ Ob, int seq, char* lds, LAS unsigned char* lds3, const int wave_) {
;   const int wid = wave_, lane = lane_id_(), tid = wid * 64 + lane, r32 = lane & 31, hi = lane >> 5;
;   bf16_t* V_lds = (bf16_t*)lds; bf16_t* K_lds = (bf16_t*)(lds + 2 * SHM_V);
;   float* ws = (float*)(lds + 2 * SHM_V + 2 * SHM_K) + wid * 64; float* li_l = ws; float* al_l = ws + 32;
;   float m_reg = -1e30f, l_reg = 0; f32x16 o[4] = {}; bf16x8 qr[8];
;   const bf16_t* Qw = Qb + (long)(wid * QBLK + r32) * LDQ + hi * 8;
; #pragma unroll
;   for (int d0 = 0; d0 < 8; ++d0) qr[d0] = *reinterpret_cast<const bf16x8*>(Qw + d0 * 16);
;   const int sr = tid >> 4, sc = (tid & 15) * 8, vst0 = v_st(sr, sc), vst1 = v_st(32 + sr, sc);
;   const int vb0 = (int)(uintptr_t)V_lds + v_rd_base(lane);
;   struct { bf16x8 vs0, vs1, ks0, ks1; } sr_[2];
;     ...
;   f32x16 pA0, pA1, pB0, pB1; float mnA, mnB, alA, alB; bf16x8 pa0, pa1, pa2, pa3; const int NT = seq / KVBLK;
;   constexpr int SE = 0, SO = 1;
	s_nop 0
	v_mfma_f32_32x32x16_bf16 v[0:15], v[160:163], v[210:213], v[0:15]
	ds_read_b64_tr_b16 v[210:211], v190 offset:0x200
	ds_read_b64_tr_b16 v[212:213], v190 offset:0xa00
	v_mfma_f32_32x32x16_bf16 v[0:15], v[164:167], v[214:217], v[0:15]
	ds_read_b64_tr_b16 v[214:215], v190 offset:0x1200
	ds_read_b64_tr_b16 v[216:217], v190 offset:0x1a00
	v_mfma_f32_32x32x16_bf16 v[0:15], v[170:173], v[218:221], v[0:15]
	ds_read_b64_tr_b16 v[218:219], v190 offset:0x2200
	ds_read_b64_tr_b16 v[220:221], v190 offset:0x2a00
	v_mfma_f32_32x32x16_bf16 v[0:15], v[206:209], v[222:225], v[0:15]
	ds_read_b64_tr_b16 v[222:223], v190 offset:0x3200
	ds_read_b64_tr_b16 v[224:225], v190 offset:0x3a00
	s_waitcnt lgkmcnt(0)
	v_mfma_f32_32x32x16_bf16 v[48:63], v[160:163], v[210:213], v[48:63]
	ds_read_b64_tr_b16 v[210:211], v190 offset:0x400
	ds_read_b64_tr_b16 v[212:213], v190 offset:0xc00
	v_mfma_f32_32x32x16_bf16 v[48:63], v[164:167], v[214:217], v[48:63]
	ds_read_b64_tr_b16 v[214:215], v190 offset:0x1400
	ds_read_b64_tr_b16 v[216:217], v190 offset:0x1c00
	v_mfma_f32_32x32x16_bf16 v[48:63], v[170:173], v[218:221], v[48:63]
	ds_read_b64_tr_b16 v[218:219], v190 offset:0x2400
	ds_read_b64_tr_b16 v[220:221], v190 offset:0x2c00
	v_mfma_f32_32x32x16_bf16 v[48:63], v[206:209], v[222:225], v[48:63]
	ds_read_b64_tr_b16 v[222:223], v190 offset:0x3400
	ds_read_b64_tr_b16 v[224:225], v190 offset:0x3c00
	s_waitcnt lgkmcnt(0)
	v_mfma_f32_32x32x16_bf16 v[32:47], v[160:163], v[210:213], v[32:47]
	ds_read_b64_tr_b16 v[210:211], v190 offset:0x600
	ds_read_b64_tr_b16 v[212:213], v190 offset:0xe00
	v_mfma_f32_32x32x16_bf16 v[32:47], v[164:167], v[214:217], v[32:47]
	ds_read_b64_tr_b16 v[214:215], v190 offset:0x1600
	ds_read_b64_tr_b16 v[216:217], v190 offset:0x1e00
	v_mfma_f32_32x32x16_bf16 v[32:47], v[170:173], v[218:221], v[32:47]
	ds_read_b64_tr_b16 v[218:219], v190 offset:0x2600
	ds_read_b64_tr_b16 v[220:221], v190 offset:0x2e00
	v_mfma_f32_32x32x16_bf16 v[32:47], v[206:209], v[222:225], v[32:47]
	ds_read_b64_tr_b16 v[222:223], v190 offset:0x3600
	ds_read_b64_tr_b16 v[224:225], v190 offset:0x3e00
	s_waitcnt lgkmcnt(0)
	v_mfma_f32_32x32x16_bf16 v[16:31], v[160:163], v[210:213], v[16:31]
	v_max_f32_e32 v160, v81, v81
	v_max_f32_e32 v161, v80, v80
	v_max_f32_e32 v160, v161, v160
	v_max3_f32 v160, v160, v82, v83
	v_max3_f32 v160, v160, v84, v85
	v_max3_f32 v160, v160, v86, v87
	v_max3_f32 v160, v160, v88, v89
	v_max3_f32 v160, v160, v90, v91
	v_max3_f32 v160, v160, v92, v93
	v_mfma_f32_32x32x16_bf16 v[16:31], v[164:167], v[214:217], v[16:31]
	v_max3_f32 v160, v160, v94, v95
	v_max3_f32 v160, v160, v64, v65
	v_max3_f32 v160, v160, v66, v67
	v_max3_f32 v160, v160, v68, v69
	v_max3_f32 v160, v160, v70, v71
	v_max3_f32 v160, v160, v72, v73
	v_max3_f32 v160, v160, v74, v75
	v_max3_f32 v160, v160, v76, v77
	v_mfma_f32_32x32x16_bf16 v[16:31], v[170:173], v[218:221], v[16:31]
	v_max3_f32 v160, v160, v78, v79
	v_mov_b32_e32 v161, v160
	s_nop 1
	v_permlane32_swap_b32_e32 v160, v161
	v_max_f32_e32 v161, v161, v161
	v_max_f32_e32 v160, v160, v160
	v_max_f32_e32 v160, v160, v161
	v_sub_f32_e32 v161, v160, v168
	v_cmp_ge_f32_e32 vcc, s52, v161
	v_max_f32_e32 v161, v168, v168
	v_max_f32_e32 v160, v161, v160
	v_mfma_f32_32x32x16_bf16 v[16:31], v[206:209], v[222:225], v[16:31]
	v_sub_f32_e32 v161, v168, v160
	v_mul_f32_e32 v161, 0x3e0293ee, v161
	v_exp_f32_e32 v161, v161
	s_cmp_eq_u64 vcc, exec
	s_cselect_b64 s[4:5], -1, 0
	s_barrier
	s_waitcnt vmcnt(8)
	v_cndmask_b32_e64 v206, v161, 1.0, s[4:5]
	v_cmp_gt_f32_e32 vcc, 1.0, v206
	s_waitcnt vmcnt(8)
	ds_write_b128 v193, v[128:131]
	ds_write_b128 v194, v[132:135]
	ds_write_b128 v191, v[136:139] offset:32768
	ds_write_b128 v199, v[140:143] offset:32768
	s_cbranch_vccz .LBB0_514
	s_and_saveexec_b64 s[34:35], s[2:3]
	ds_write_b32 v187, v206 offset:128
	s_or_b64 exec, exec, s[34:35]
	s_waitcnt lgkmcnt(0)
	v_add_u32_e32 v161, s29, v176
	ds_read_b128 v[162:165], v161 offset:224
	ds_read_b128 v[170:173], v161 offset:192
	ds_read_b128 v[208:211], v161 offset:160
	ds_read_b128 v[212:215], v161 offset:128
	s_waitcnt lgkmcnt(3)
	v_pk_mul_f32 v[12:13], v[12:13], v[162:163]
	s_waitcnt lgkmcnt(2)
	v_pk_mul_f32 v[8:9], v[8:9], v[170:171]
	s_waitcnt lgkmcnt(1)
	v_pk_mul_f32 v[4:5], v[4:5], v[208:209]
	v_pk_mul_f32 v[14:15], v[14:15], v[164:165]
	v_pk_mul_f32 v[10:11], v[10:11], v[172:173]
	v_pk_mul_f32 v[6:7], v[6:7], v[210:211]
	s_waitcnt lgkmcnt(0)
	v_pk_mul_f32 v[2:3], v[2:3], v[214:215]
	v_pk_mul_f32 v[0:1], v[0:1], v[212:213]
	v_pk_mul_f32 v[60:61], v[60:61], v[162:163]
	v_pk_mul_f32 v[56:57], v[56:57], v[170:171]
	v_pk_mul_f32 v[52:53], v[52:53], v[208:209]
	v_pk_mul_f32 v[62:63], v[62:63], v[164:165]
	v_pk_mul_f32 v[58:59], v[58:59], v[172:173]
	v_pk_mul_f32 v[54:55], v[54:55], v[210:211]
	v_pk_mul_f32 v[50:51], v[50:51], v[214:215]
	v_pk_mul_f32 v[48:49], v[48:49], v[212:213]
	v_pk_mul_f32 v[44:45], v[44:45], v[162:163]
	v_pk_mul_f32 v[40:41], v[40:41], v[170:171]
	v_pk_mul_f32 v[36:37], v[36:37], v[208:209]
	v_pk_mul_f32 v[46:47], v[46:47], v[164:165]
	v_pk_mul_f32 v[42:43], v[42:43], v[172:173]
	v_pk_mul_f32 v[38:39], v[38:39], v[210:211]
	v_pk_mul_f32 v[34:35], v[34:35], v[214:215]
	v_pk_mul_f32 v[32:33], v[32:33], v[212:213]
	v_pk_mul_f32 v[28:29], v[28:29], v[162:163]
	v_pk_mul_f32 v[24:25], v[24:25], v[170:171]
	v_pk_mul_f32 v[20:21], v[20:21], v[208:209]
	v_pk_mul_f32 v[30:31], v[30:31], v[164:165]
	v_pk_mul_f32 v[26:27], v[26:27], v[172:173]
	v_pk_mul_f32 v[22:23], v[22:23], v[210:211]
	v_pk_mul_f32 v[18:19], v[18:19], v[214:215]
	v_pk_mul_f32 v[16:17], v[16:17], v[212:213]

; #define LAS __attribute__((address_space(3)))
; template <int D0> __device__ __forceinline__ void pv_one(f32x16& od, int vb, bf16x8 pa0, bf16x8 pa1, bf16x8 pa2, bf16x8 pa3) {
;   const s16x4 l0 = tr_read<v_rd_off(D0, 0, 0)>(vb), h0 = tr_read<v_rd_off(D0, 0, 1)>(vb), l1 = tr_read<v_rd_off(D0, 1, 0)>(vb), h1 = tr_read<v_rd_off(D0, 1, 1)>(vb);
;   const s16x4 l2 = tr_read<v_rd_off(D0, 2, 0)>(vb), h2 = tr_read<v_rd_off(D0, 2, 1)>(vb), l3 = tr_read<v_rd_off(D0, 3, 0)>(vb), h3 = tr_read<v_rd_off(D0, 3, 1)>(vb);
;   asm volatile("s_waitcnt lgkmcnt(0)" ::: "memory"); SBAR();
;     ...
;   od = __builtin_amdgcn_mfma_f32_32x32x16_bf16(pa0, PK(l0, h0), od, 0, 0, 0);
;   od = __builtin_amdgcn_mfma_f32_32x32x16_bf16(pa1, PK(l1, h1), od, 0, 0, 0);
;   od = __builtin_amdgcn_mfma_f32_32x32x16_bf16(pa2, PK(l2, h2), od, 0, 0, 0);
;   od = __builtin_amdgcn_mfma_f32_32x32x16_bf16(pa3, PK(l3, h3), od, 0, 0, 0);
;     ...
; }
; __device__ __forceinline__ void pv_d0(f32x16* o, int vb, bf16x8 pa0, bf16x8 pa1, bf16x8 pa2, bf16x8 pa3) {
;   pv_one<0>(o[0], vb, pa0, pa1, pa2, pa3); pv_one<1>(o[1], vb, pa0, pa1, pa2, pa3); pv_one<2>(o[2], vb, pa0, pa1, pa2, pa3); pv_one<3>(o[3], vb, pa0, pa1, pa2, pa3);
; }
; __device__ __forceinline__ void attn_dense_body(const bf16_t* __restrict__ Qb, const bf16_t* __restrict__ Kh, const bf16_t* __restrict__ Vh,
;                                                 unsigned char* __restrict__ Ob, int seq, char* lds, LAS unsigned char* lds3, const int wave_) {
;   const int wid = wave_, lane = lane_id_(), tid = wid * 64 + lane, r32 = lane & 31, hi = lane >> 5;
;   bf16_t* V_lds = (bf16_t*)lds; bf16_t* K_lds = (bf16_t*)(lds + 2 * SHM_V);
;   float* ws = (float*)(lds + 2 * SHM_V + 2 * SHM_K) + wid * 64; float* li_l = ws; float* al_l = ws + 32;
;   float m_reg = -1e30f, l_reg = 0; f32x16 o[4] = {}; bf16x8 qr[8];
;   const bf16_t* Qw = Qb + (long)(wid * QBLK + r32) * LDQ + hi * 8;
; #pragma unroll
;   for (int d0 = 0; d0 < 8; ++d0) qr[d0] = *reinterpret_cast<const bf16x8*>(Qw + d0 * 16);
;   const int sr = tid >> 4, sc = (tid & 15) * 8, vst0 = v_st(sr, sc), vst1 = v_st(32 + sr, sc);
;   const int vb0 = (int)(uintptr_t)V_lds + v_rd_base(lane);
;   struct { bf16x8 vs0, vs1, ks0, ks1; } sr_[2];
;     ...
;   f32x16 pA0, pA1, pB0, pB1; float mnA, mnB, alA, alB; bf16x8 pa0, pa1, pa2, pa3; const int NT = seq / KVBLK;
;   constexpr int SE = 0, SO = 1;
.LBB0_516:
	ds_read_b64_tr_b16 v[210:211], v189 offset:0
	ds_read_b64_tr_b16 v[212:213], v189 offset:0x800
	ds_read_b64_tr_b16 v[214:215], v189 offset:0x1000
	ds_read_b64_tr_b16 v[216:217], v189 offset:0x1800
	ds_read_b64_tr_b16 v[218:219], v189 offset:0x2000
	ds_read_b64_tr_b16 v[220:221], v189 offset:0x2800
	ds_read_b64_tr_b16 v[222:223], v189 offset:0x3000
	ds_read_b64_tr_b16 v[224:225], v189 offset:0x3800
	s_waitcnt lgkmcnt(0)
	s_nop 0
	v_mfma_f32_32x32x16_bf16 v[0:15], v[160:163], v[210:213], v[0:15]
	ds_read_b64_tr_b16 v[210:211], v189 offset:0x200
	ds_read_b64_tr_b16 v[212:213], v189 offset:0xa00
	v_mfma_f32_32x32x16_bf16 v[0:15], v[164:167], v[214:217], v[0:15]
	ds_read_b64_tr_b16 v[214:215], v189 offset:0x1200
	ds_read_b64_tr_b16 v[216:217], v189 offset:0x1a00
	v_mfma_f32_32x32x16_bf16 v[0:15], v[168:171], v[218:221], v[0:15]
	ds_read_b64_tr_b16 v[218:219], v189 offset:0x2200
	ds_read_b64_tr_b16 v[220:221], v189 offset:0x2a00
	v_mfma_f32_32x32x16_bf16 v[0:15], v[172:175], v[222:225], v[0:15]
	ds_read_b64_tr_b16 v[222:223], v189 offset:0x3200
	ds_read_b64_tr_b16 v[224:225], v189 offset:0x3a00
	s_waitcnt lgkmcnt(0)
	v_mfma_f32_32x32x16_bf16 v[48:63], v[160:163], v[210:213], v[48:63]
	ds_read_b64_tr_b16 v[210:211], v189 offset:0x400
	ds_read_b64_tr_b16 v[212:213], v189 offset:0xc00
	v_mfma_f32_32x32x16_bf16 v[48:63], v[164:167], v[214:217], v[48:63]
	ds_read_b64_tr_b16 v[214:215], v189 offset:0x1400
	ds_read_b64_tr_b16 v[216:217], v189 offset:0x1c00
	v_mfma_f32_32x32x16_bf16 v[48:63], v[168:171], v[218:221], v[48:63]
	ds_read_b64_tr_b16 v[218:219], v189 offset:0x2400
	ds_read_b64_tr_b16 v[220:221], v189 offset:0x2c00
	v_mfma_f32_32x32x16_bf16 v[48:63], v[172:175], v[222:225], v[48:63]
	ds_read_b64_tr_b16 v[222:223], v189 offset:0x3400
	ds_read_b64_tr_b16 v[224:225], v189 offset:0x3c00
	s_waitcnt lgkmcnt(0)
	v_mfma_f32_32x32x16_bf16 v[32:47], v[160:163], v[210:213], v[32:47]
	ds_read_b64_tr_b16 v[210:211], v189 offset:0x600
	ds_read_b64_tr_b16 v[212:213], v189 offset:0xe00
	v_mfma_f32_32x32x16_bf16 v[32:47], v[164:167], v[214:217], v[32:47]
	ds_read_b64_tr_b16 v[214:215], v189 offset:0x1600
	ds_read_b64_tr_b16 v[216:217], v189 offset:0x1e00
	v_mfma_f32_32x32x16_bf16 v[32:47], v[168:171], v[218:221], v[32:47]
	ds_read_b64_tr_b16 v[218:219], v189 offset:0x2600
	ds_read_b64_tr_b16 v[220:221], v189 offset:0x2e00
	v_mfma_f32_32x32x16_bf16 v[32:47], v[172:175], v[222:225], v[32:47]
	ds_read_b64_tr_b16 v[222:223], v189 offset:0x3600
	ds_read_b64_tr_b16 v[224:225], v189 offset:0x3e00
	s_waitcnt lgkmcnt(0)
	v_mfma_f32_32x32x16_bf16 v[16:31], v[160:163], v[210:213], v[16:31]
	v_max_f32_e32 v160, v81, v81
	v_max_f32_e32 v161, v80, v80
	v_max_f32_e32 v160, v161, v160
	v_max3_f32 v160, v160, v82, v83
	v_max3_f32 v160, v160, v84, v85
	v_max3_f32 v160, v160, v86, v87
	v_max3_f32 v160, v160, v88, v89
	v_max3_f32 v160, v160, v90, v91
	v_max3_f32 v160, v160, v92, v93
	v_mfma_f32_32x32x16_bf16 v[16:31], v[164:167], v[214:217], v[16:31]
	v_max3_f32 v160, v160, v94, v95
	v_max3_f32 v160, v160, v64, v65
	v_max3_f32 v160, v160, v66, v67
	v_max3_f32 v160, v160, v68, v69
	v_max3_f32 v160, v160, v70, v71
	v_max3_f32 v160, v160, v72, v73
	v_max3_f32 v160, v160, v74, v75
	v_max3_f32 v160, v160, v76, v77
	v_mfma_f32_32x32x16_bf16 v[16:31], v[168:171], v[218:221], v[16:31]
	v_max3_f32 v160, v160, v78, v79
	v_mov_b32_e32 v161, v160
	s_nop 1
	v_permlane32_swap_b32_e32 v160, v161
	v_max_f32_e32 v161, v161, v161
	v_max_f32_e32 v160, v160, v160
	v_max_f32_e32 v160, v160, v161
	v_sub_f32_e32 v161, v160, v207
	v_cmp_ge_f32_e32 vcc, s52, v161
	v_max_f32_e32 v161, v207, v207
	v_max_f32_e32 v161, v161, v160
	v_mfma_f32_32x32x16_bf16 v[16:31], v[172:175], v[222:225], v[16:31]
	v_sub_f32_e32 v160, v207, v161
	v_mul_f32_e32 v160, 0x3e0293ee, v160
	v_exp_f32_e32 v160, v160
	s_cmp_eq_u64 vcc, exec
	s_cselect_b64 s[4:5], -1, 0
	s_barrier
	s_waitcnt vmcnt(8)
	v_cndmask_b32_e64 v160, v160, 1.0, s[4:5]
	v_cmp_gt_f32_e32 vcc, 1.0, v160
	ds_write_b128 v193, v[144:147] offset:16384
	ds_write_b128 v194, v[148:151] offset:16384
	ds_write_b128 v191, v[152:155] offset:49152
	ds_write_b128 v199, v[156:159] offset:49152
	s_cbranch_vccz .LBB0_520
	s_and_saveexec_b64 s[34:35], s[2:3]
	ds_write_b32 v187, v160 offset:128
	s_or_b64 exec, exec, s[34:35]
	s_waitcnt lgkmcnt(0)
	v_add_u32_e32 v156, s29, v176
	ds_read_b128 v[144:147], v156 offset:224
	ds_read_b128 v[148:151], v156 offset:192
	ds_read_b128 v[152:155], v156 offset:160
	ds_read_b128 v[156:159], v156 offset:128
	s_waitcnt lgkmcnt(3)
	v_pk_mul_f32 v[12:13], v[12:13], v[144:145]
	s_waitcnt lgkmcnt(2)
	v_pk_mul_f32 v[8:9], v[8:9], v[148:149]
	s_waitcnt lgkmcnt(1)
	v_pk_mul_f32 v[4:5], v[4:5], v[152:153]
	v_pk_mul_f32 v[14:15], v[14:15], v[146:147]
	v_pk_mul_f32 v[10:11], v[10:11], v[150:151]
	v_pk_mul_f32 v[6:7], v[6:7], v[154:155]
	s_waitcnt lgkmcnt(0)
	v_pk_mul_f32 v[2:3], v[2:3], v[158:159]
	v_pk_mul_f32 v[0:1], v[0:1], v[156:157]
	v_pk_mul_f32 v[60:61], v[60:61], v[144:145]
	v_pk_mul_f32 v[56:57], v[56:57], v[148:149]
	v_pk_mul_f32 v[52:53], v[52:53], v[152:153]
	v_pk_mul_f32 v[62:63], v[62:63], v[146:147]
	v_pk_mul_f32 v[58:59], v[58:59], v[150:151]
	v_pk_mul_f32 v[54:55], v[54:55], v[154:155]
	v_pk_mul_f32 v[50:51], v[50:51], v[158:159]
	v_pk_mul_f32 v[48:49], v[48:49], v[156:157]
	v_pk_mul_f32 v[44:45], v[44:45], v[144:145]
	v_pk_mul_f32 v[40:41], v[40:41], v[148:149]
	v_pk_mul_f32 v[36:37], v[36:37], v[152:153]
	v_pk_mul_f32 v[46:47], v[46:47], v[146:147]
	v_pk_mul_f32 v[42:43], v[42:43], v[150:151]
	v_pk_mul_f32 v[38:39], v[38:39], v[154:155]
	v_pk_mul_f32 v[34:35], v[34:35], v[158:159]
	v_pk_mul_f32 v[32:33], v[32:33], v[156:157]
	v_pk_mul_f32 v[28:29], v[28:29], v[144:145]
	v_pk_mul_f32 v[24:25], v[24:25], v[148:149]
	v_pk_mul_f32 v[20:21], v[20:21], v[152:153]
	v_pk_mul_f32 v[30:31], v[30:31], v[146:147]
	v_pk_mul_f32 v[26:27], v[26:27], v[150:151]
	v_pk_mul_f32 v[22:23], v[22:23], v[154:155]
	v_pk_mul_f32 v[18:19], v[18:19], v[158:159]
	v_pk_mul_f32 v[16:17], v[16:17], v[156:157]
; __device__ __forceinline__ void partialSM(f32x16& p0, f32x16& p1, float& m_reg, float& mn, float& alpha) {
;     ...
;   if (__builtin_expect(__all(pmax - m_reg <= THR / SCALE), 1)) { mn = m_reg; alpha = 1.f; }
;   else { mn = fmaxf(m_reg, pmax); alpha = __builtin_amdgcn_exp2f((m_reg - mn) * C); m_reg = mn; }
;   float mnC = -mn * C;
; #pragma unroll
;   for (int r = 0; r < 16; ++r) p0[r] = fmaf(p0[r], C, mnC);
; #pragma unroll
;   for (int r = 0; r < 16; ++r) p1[r] = fmaf(p1[r], C, mnC);
; #pragma unroll
;   for (int r = 0; r < 16; ++r) p0[r] = __builtin_amdgcn_exp2f(p0[r]);
; }
; __device__ __forceinline__ void finishSM(f32x16& p0, f32x16& p1, float alpha, float& l_reg, bf16x8& pa0, bf16x8& pa1, bf16x8& pa2, bf16x8& pa3) {
; #pragma unroll
;   for (int r = 0; r < 16; ++r) p1[r] = __builtin_amdgcn_exp2f(p1[r]);
;   float ps = 0;
; #pragma unroll
;   for (int r = 0; r < 16; ++r) ps += p0[r];
; #pragma unroll
;   for (int r = 0; r < 16; ++r) ps += p1[r];
;   { auto rr = __builtin_amdgcn_permlane32_swap(__float_as_uint(ps), __float_as_uint(ps), false, false);
;     ps = __uint_as_float(rr[0]) + __uint_as_float(rr[1]); }
;   l_reg = l_reg * alpha + ps;
.LBB0_520:
	v_cndmask_b32_e64 v168, v161, v207, s[4:5]
	v_mul_f32_e32 v150, 0xbe0293ee, v168
	v_mov_b32_e32 v151, v150
	v_fmamk_f32 v80, v80, 0x3e0293ee, v150
	v_fmamk_f32 v81, v81, 0x3e0293ee, v150
	v_fmamk_f32 v82, v82, 0x3e0293ee, v150
	v_fmamk_f32 v83, v83, 0x3e0293ee, v150
	v_fmamk_f32 v84, v84, 0x3e0293ee, v150
	v_fmamk_f32 v85, v85, 0x3e0293ee, v150
	v_fmamk_f32 v86, v86, 0x3e0293ee, v150
	v_fmamk_f32 v87, v87, 0x3e0293ee, v150
	v_fmamk_f32 v88, v88, 0x3e0293ee, v150
	v_fmamk_f32 v89, v89, 0x3e0293ee, v150
	v_fmamk_f32 v90, v90, 0x3e0293ee, v150
	v_fmamk_f32 v91, v91, 0x3e0293ee, v150
	v_fmamk_f32 v92, v92, 0x3e0293ee, v150
	v_fmamk_f32 v93, v93, 0x3e0293ee, v150
	v_fmamk_f32 v94, v94, 0x3e0293ee, v150
	v_fmac_f32_e32 v151, 0x3e0293ee, v95
	v_exp_f32_e32 v175, v80
	v_exp_f32_e32 v210, v81
	v_exp_f32_e32 v161, v82
	v_exp_f32_e32 v207, v83
	v_exp_f32_e32 v162, v84
	v_exp_f32_e32 v174, v85
	v_exp_f32_e32 v163, v86
	v_exp_f32_e32 v173, v87
	v_exp_f32_e32 v164, v88
	v_exp_f32_e32 v172, v89
	v_exp_f32_e32 v165, v90
	v_exp_f32_e32 v171, v91
	v_exp_f32_e32 v166, v92
	v_exp_f32_e32 v170, v93
	v_exp_f32_e32 v167, v94
	v_exp_f32_e32 v169, v151
	v_pk_fma_f32 v[156:157], v[64:65], s[28:29], v[150:151] op_sel_hi:[1,0,0]
	v_add_f32_e32 v64, v204, v205
	v_fmac_f32_e32 v64, v203, v188
	v_add_f32_e32 v188, v208, v209
	v_pk_fma_f32 v[154:155], v[66:67], s[28:29], v[150:151] op_sel_hi:[1,0,0]
	v_pk_fma_f32 v[148:149], v[68:69], s[28:29], v[150:151] op_sel_hi:[1,0,0]
	v_pk_fma_f32 v[146:147], v[70:71], s[28:29], v[150:151] op_sel_hi:[1,0,0]
	v_pk_fma_f32 v[144:145], v[72:73], s[28:29], v[150:151] op_sel_hi:[1,0,0]
	v_pk_fma_f32 v[158:159], v[74:75], s[28:29], v[150:151] op_sel_hi:[1,0,0]
	v_pk_fma_f32 v[152:153], v[76:77], s[28:29], v[150:151] op_sel_hi:[1,0,0]
	v_pk_fma_f32 v[150:151], v[78:79], s[28:29], v[150:151] op_sel_hi:[1,0,0]
	v_fmac_f32_e32 v188, v64, v206
	s_and_b64 vcc, exec, s[80:81]
	s_cbranch_vccnz .Latt_cv_w0
	s_waitcnt vmcnt(4)
	s_branch .Latt_cv_wd

; #define SBAR() __builtin_amdgcn_sched_barrier(0)
; #define SLOAD(i, k0) do { sr_[i].vs0 = *reinterpret_cast<const bf16x8*>(&Vh[(long)((k0) + sr) * LDK + sc]); sr_[i].vs1 = *reinterpret_cast<const bf16x8*>(&Vh[(long)((k0) + 32 + sr) * LDK + sc]); \
;     sr_[i].ks0 = *reinterpret_cast<const bf16x8*>(&Kh[(long)((k0) + sr) * LDK + sc]); sr_[i].ks1 = *reinterpret_cast<const bf16x8*>(&Kh[(long)((k0) + 32 + sr) * LDK + sc]); } while (0)
; #define SWRITE(b, i) do { *(bf16x8*)((char*)V_lds + (b) * SHM_V + vst0) = sr_[i].vs0;          \
;     *(bf16x8*)((char*)V_lds + (b) * SHM_V + vst1) = sr_[i].vs1; int kc = sc * 2;               \
;     *(bf16x8*)((char*)K_lds + (b) * SHM_K + KSWZ(sr, kc)) = sr_[i].ks0;                       \
;     *(bf16x8*)((char*)K_lds + (b) * SHM_K + KSWZ(32 + sr, kc)) = sr_[i].ks1; } while (0)
; #define SWAIT() do { asm volatile("s_waitcnt vmcnt(4)" ::: "memory"); } while (0)
; #define RESC(a) do { if (__any((a) < 1.f)) { if (hi == 0) al_l[r32] = (a); asm volatile("s_waitcnt lgkmcnt(0)" ::: "memory"); \
;     _Pragma("unroll") for (int d = 0; d < 4; ++d) _Pragma("unroll") for (int r = 0; r < 16; ++r) o[d][r] *= al_l[crow(r, hi)]; } } while (0)
; __device__ __forceinline__ void attn_dense_body(const bf16_t* __restrict__ Qb, const bf16_t* __restrict__ Kh, const bf16_t* __restrict__ Vh,
;                                                 unsigned char* __restrict__ Ob, int seq, char* lds, LAS unsigned char* lds3, const int wave_) {
;     ...
;   for (int j = 1; j + 1 < NT; j += 2) {
;     SBAR(); qkt(pB0, pB1, (bf16_t*)((char*)K_lds + SHM_K), qr, r32, hi);
;     finishSM(pA0, pA1, alA, l_reg, pa0, pa1, pa2, pa3); SBAR();
;     SLOAD(SO, (j + 2) * KVBLK); SBAR();
;     pv_d0(o, vb0, pa0, pa1, pa2, pa3); partialSM(pB0, pB1, m_reg, mnB, alB);
;     __syncthreads(); SWAIT(); SWRITE(0, SE);
;     RESC(alB); __syncthreads();
;     SBAR(); qkt(pA0, pA1, K_lds, qr, r32, hi);
;     finishSM(pB0, pB1, alB, l_reg, pa0, pa1, pa2, pa3); SBAR();
;     if (j + 3 < NT) SLOAD(SE, (j + 3) * KVBLK); SBAR();
;     pv_d0(o, vb0 + (int)SHM_V, pa0, pa1, pa2, pa3); partialSM(pA0, pA1, m_reg, mnA, alA);
;     __syncthreads(); SWAIT(); SWRITE(1, SO);
;     RESC(alA); __syncthreads();
;   }
.Latt_cv_wd:
	s_lshr_b32 s100, s53, 8
	s_lshl_b32 s100, s100, 4
	s_add_i32 s100, s100, 16
	s_cmp_lt_u32 s99, s100
	s_cbranch_scc0 .Latt_cv_skip
	v_mul_f32_e32 v232, 0x42000000, v232
	v_mul_f32_e32 v236, 0x42000000, v236
	v_mul_f32_e32 v240, 0x42000000, v240
	v_mul_f32_e32 v244, 0x42000000, v244
	v_mov_b32_e32 v248, 0
	v_cvt_pk_fp8_f32 v248, v232, v236
	v_cvt_pk_fp8_f32 v248, v240, v244 op_sel:[0,0,1]
	v_mul_f32_e32 v233, 0x42000000, v233
	v_mul_f32_e32 v237, 0x42000000, v237
	v_mul_f32_e32 v241, 0x42000000, v241
	v_mul_f32_e32 v245, 0x42000000, v245
	v_mov_b32_e32 v249, 0
	v_cvt_pk_fp8_f32 v249, v233, v237
	v_cvt_pk_fp8_f32 v249, v241, v245 op_sel:[0,0,1]
	v_mul_f32_e32 v234, 0x42000000, v234
	v_mul_f32_e32 v238, 0x42000000, v238
	v_mul_f32_e32 v242, 0x42000000, v242
	v_mul_f32_e32 v246, 0x42000000, v246
	v_mov_b32_e32 v250, 0
	v_cvt_pk_fp8_f32 v250, v234, v238
	v_cvt_pk_fp8_f32 v250, v242, v246 op_sel:[0,0,1]
	v_mul_f32_e32 v235, 0x42000000, v235
	v_mul_f32_e32 v239, 0x42000000, v239
	v_mul_f32_e32 v243, 0x42000000, v243
	v_mul_f32_e32 v247, 0x42000000, v247
	v_mov_b32_e32 v251, 0
	v_cvt_pk_fp8_f32 v251, v235, v239
	v_cvt_pk_fp8_f32 v251, v243, v247 op_sel:[0,0,1]
	v_mbcnt_lo_u32_b32 v253, -1, 0
	v_mbcnt_hi_u32_b32 v253, -1, v253
	v_lshlrev_b32_e32 v252, 6, v253
	s_and_b32 s100, s98, 7
	s_lshl_b32 s100, s100, 12
	s_add_i32 s100, s100, 0x11000
	s_and_b32 s101, s99, 3
	s_lshl_b32 s101, s101, 2
	s_add_i32 s100, s100, s101
	v_add_u32_e32 v252, s100, v252
	ds_write_b32 v252, v248
	ds_write_b32 v252, v249 offset:16
	ds_write_b32 v252, v250 offset:32
	ds_write_b32 v252, v251 offset:48
	s_cmp_eq_u32 s101, 12
	s_cbranch_scc0 .Latt_cv_nostore
	v_add_u32_e32 v252, -12, v252
	s_waitcnt lgkmcnt(0)
	ds_read_b128 v[232:235], v252
	ds_read_b128 v[236:239], v252 offset:16
	ds_read_b128 v[240:243], v252 offset:32
	ds_read_b128 v[244:247], v252 offset:48
	s_lshr_b32 s100, s99, 2
	s_add_i32 s100, s100, 32
	s_lshl_b32 s100, s100, 11
	s_and_b32 s101, s98, 0x7ff
	s_add_i32 s100, s100, s101
	s_sub_i32 s101, s100, 0x10000
	s_lshr_b32 s101, s101, 10
	s_lshl_b32 s101, s101, 22
	v_mov_b32_e32 v248, s101
	s_and_b32 s101, s100, 63
	s_lshl_b32 s101, s101, 16
	v_add_u32_e32 v248, s101, v248
	s_bfe_u32 s101, s100, 0x40006
	s_lshl_b32 s101, s101, 7
	v_add_u32_e32 v248, s101, v248
	v_lshrrev_b32_e32 v249, 3, v253
	v_and_b32_e32 v250, 7, v253
	v_lshl_add_u32 v248, v249, 4, v248
	v_lshl_add_u32 v248, v250, 13, v248
	v_readlane_b32 s100, v254, 48
	v_readlane_b32 s101, v254, 49
	s_add_u32 s100, s100, 0x14d59400
	s_addc_u32 s101, s101, 0
	s_waitcnt lgkmcnt(0)
	global_store_dwordx4 v248, v[232:235], s[100:101]
	global_store_dwordx4 v248, v[236:239], s[100:101] offset:2048
	v_add_u32_e32 v249, 0x1000, v248
	global_store_dwordx4 v249, v[240:243], s[100:101]
	global_store_dwordx4 v249, v[244:247], s[100:101] offset:2048
.Latt_cv_nostore:
	s_add_i32 s99, s99, 1
.Latt_cv_skip:
	s_add_i32 s36, s36, 2
	v_lshl_add_u64 v[178:179], v[178:179], 0, s[30:31]
	s_and_b64 vcc, exec, s[80:81]
	s_waitcnt lgkmcnt(0)
	s_barrier
	s_cbranch_vccnz .LBB0_522
	v_mov_b32_e32 v203, v160
	s_branch .LBB0_510
.Latt_cv_nose:
	s_waitcnt vmcnt(4)
	s_branch .LBB0_516

; #define LAS __attribute__((address_space(3)))
; __device__ __forceinline__ int lane_id_() { int l; asm volatile("v_mbcnt_lo_u32_b32 %0, -1, 0\n\tv_mbcnt_hi_u32_b32 %0, -1, %0" : "=v"(l)); return l; }
; __device__ __forceinline__ void mlstm_unit(LAS unsigned char* lds, const bf16_t* __restrict__ PM, const float* __restrict__ GATES, bf16_t* __restrict__ Hout,
;                                            int b, int h, int dir, int vs, Conv& cvs, const int wave_) {
;     f32x4 cv[16];
;     const int w = wave_, lane = lane_id_(), tid = w * 64 + lane, g = lane >> 4, i16 = lane & 15, q4 = i16 >> 2, p4 = lane & 3;
;     const int sr = tid >> 3, c8 = tid & 7;
;     f32x4 accC[2][4];
; #pragma unroll
;     for (int a = 0; a < 2; ++a)
; #pragma unroll
;         for (int v = 0; v < 4; ++v) accC[a][v] = (f32x4){0.f, 0.f, 0.f, 0.f};
;     if (tid < 256) *(LAS float*)(lds + NV + tid * 4) = 0.f;
;     float m_in = 0.f;
;     bool pend_b = false;
;     u32x4 rq[4], rk[4], rv; float g_i = 0.f, g_f = 0.f;
;     const int gi_col = (dir ? 8 : 0) + h, gf_col = (dir ? 12 : 4) + h;
;     ...
;     ML_LOAD(0);
; __global__ void __launch_bounds__(NTHREADS, 2) fwd(Args args) {
;     ...
;         if (att_first) { ATT_BLOCK(); __syncthreads(); }
; #pragma unroll 1
;         for (int rep_ = 0; rep_ < NREP(4); ++rep_) {
;             ml::Conv cvs{w_gu, w_dn, WTGU, WTDN, bx * 8 + wave, G * 8};
;             for (int un = vcu; un < 256; un += G) {
;                 const int bh = un >> 4, dir = (un >> 3) & 1, vs = un & 7;
;                 ml::mlstm_unit(lds, PM, GATES, dir ? HB : HF, bh >> 2, bh & 3, dir, vs, cvs, wave);
.LBB0_528:
	s_waitcnt vmcnt(0) lgkmcnt(0)
	s_barrier
	v_readlane_b32 s0, v255, 26
	v_readlane_b32 s1, v255, 27
	s_and_b64 vcc, exec, s[0:1]
	s_cbranch_vccnz .LBB0_659
.LBB0_529:
	s_mov_b32 s101, 0x10000
	s_bitcmp0_b32 s98, 0
	s_cselect_b32 s100, 1, 0
	s_bitcmp0_b32 s98, 1
	s_cselect_b32 s100, s100, 0
	s_bitcmp0_b32 s98, 2
	s_cselect_b32 s100, s100, 0
	s_cmp_eq_u32 s100, 1
	s_cselect_b32 s101, 0x10000, s101
	s_lshl_b32 s0, s76, 3
	s_add_i32 s33, s77, s0
	s_lshl_b32 s62, s73, 3
	v_writelane_b32 v255, s57, 28
	s_cmpk_gt_i32 s74, 0xff
	s_cbranch_scc1 .LBB0_624
	s_add_i32 s0, s84, 0
	v_writelane_b32 v255, s0, 29
	s_add_i32 s0, s0, 0x17400
	s_lshl_b32 s2, s77, 4
	v_writelane_b32 v255, s0, 30
	s_and_b32 s2, s2, 48
	v_writelane_b32 v255, s2, 31
	s_lshl_b32 s2, s2, 1
	v_readlane_b32 s3, v254, 51
	s_add_i32 s2, s2, 0
	s_lshr_b32 s0, s3, 7
	s_add_i32 s4, s2, 0x15000
	s_and_b32 s1, s0, 0x1fffffe
	v_writelane_b32 v255, s4, 32
	s_add_i32 s2, s2, 0x10800
	v_writelane_b32 v255, s2, 33
	s_lshl_b32 s2, s1, 4
	v_writelane_b32 v255, s2, 34
	s_or_b32 s2, s0, 1
	s_lshl_b32 s4, s2, 4
	s_lshl_b32 s0, s0, 4
	v_writelane_b32 v255, s4, 35
	s_or_b32 s0, s0, 16
	v_writelane_b32 v255, s0, 36
	s_lshr_b32 s0, s3, 8
	s_mulk_i32 s0, 0x4200
	s_lshl_b32 s56, s2, 6
	s_add_i32 s0, s0, 0
	s_mulk_i32 s2, 0x2100
	v_writelane_b32 v255, s0, 37
	s_add_i32 s0, s2, 0
	s_lshl_b32 s63, s1, 6
	v_writelane_b32 v255, s0, 38
	v_readlane_b32 s0, v254, 62
	v_readlane_b32 s1, v254, 63
	v_cndmask_b32_e64 v0, 0, 1, s[24:25]
	s_mov_b32 s79, 0
	v_mov_b64_e32 v[142:143], s[0:1]
	v_cmp_ne_u32_e64 s[0:1], 1, v0
	s_movk_i32 s14, 0x100
	v_mov_b32_e32 v141, 0
	v_writelane_b32 v255, s0, 39
	s_movk_i32 s89, 0x3000
	s_movk_i32 s91, 0x1000
	v_writelane_b32 v255, s1, 40
	s_add_i32 s0, 0, 0x12c00
	v_writelane_b32 v255, s0, 41
	s_add_i32 s0, 0, 0x1fe00
	v_writelane_b32 v255, s0, 42
	v_writelane_b32 v255, s66, 43
	v_mov_b32_e32 v149, 0x20300
	v_mov_b32_e32 v153, 0x1f800
	v_writelane_b32 v255, s67, 44
	v_writelane_b32 v255, s68, 45
	s_add_i32 s1, 0, 0x20200
	v_mov_b32_e32 v154, 0x41b17218
	s_mov_b32 s11, s74
	v_writelane_b32 v255, s69, 46

; #define LAS __attribute__((address_space(3)))
; __device__ __forceinline__ unsigned cvt_pk_bf16(float lo, float hi) { unsigned r; asm volatile("v_cvt_pk_bf16_f32 %0, %1, %2" : "=v"(r) : "v"(lo), "v"(hi)); return r; }
; __device__ __forceinline__ float bf_lo(unsigned w) { return __uint_as_float(w << 16); }
; __device__ __forceinline__ float bf_hi(unsigned w) { return __uint_as_float(w & 0xffff0000u); }
; __device__ __forceinline__ void mlstm_unit(LAS unsigned char* lds, const bf16_t* __restrict__ PM, const float* __restrict__ GATES, bf16_t* __restrict__ Hout,
;                                            int b, int h, int dir, int vs, Conv& cvs, const int wave_) {
;     ...
;         {
;             const float wsv = *(LAS float*)(lds + SC_WS + sr * 4);
;             u32x4 o;
;             o.x = cvt_pk_bf16(bf_lo(rv.x) * wsv, bf_hi(rv.x) * wsv); o.y = cvt_pk_bf16(bf_lo(rv.y) * wsv, bf_hi(rv.y) * wsv);
;             o.z = cvt_pk_bf16(bf_lo(rv.z) * wsv, bf_hi(rv.z) * wsv); o.w = cvt_pk_bf16(bf_lo(rv.w) * wsv, bf_hi(rv.w) * wsv);
;             *(LAS u32x4*)(lds + VWS + sr * RV + c8 * 16) = o;
;         }
;         if (pend_b) { CV_FINISH(); pend_b = false; }
.LBB0_550:
	s_or_b64 exec, exec, s[2:3]
	v_add_u32_e32 v132, 0x20000, v196
	ds_read_b32 v135, v132
	v_lshlrev_b32_e32 v132, 16, v16
	v_and_b32_e32 v133, 0xffff0000, v16
	v_lshlrev_b32_e32 v134, 16, v17
	v_and_b32_e32 v136, 0xffff0000, v18
	s_waitcnt lgkmcnt(0)
	v_mul_f32_e32 v132, v135, v132
	v_mul_f32_e32 v133, v135, v133
	v_cvt_pk_bf16_f32 v132, v132, v133
	v_mul_f32_e32 v133, v135, v134
	v_and_b32_e32 v134, 0xffff0000, v17
	v_mul_f32_e32 v134, v135, v134
	v_cvt_pk_bf16_f32 v133, v133, v134
	v_lshlrev_b32_e32 v134, 16, v18
	v_mul_f32_e32 v134, v135, v134
	v_mul_f32_e32 v136, v135, v136
	v_cvt_pk_bf16_f32 v134, v134, v136
	v_lshlrev_b32_e32 v136, 16, v19
	v_and_b32_e32 v137, 0xffff0000, v19
	v_mul_f32_e32 v136, v135, v136
	v_mul_f32_e32 v135, v135, v137
	s_andn2_b64 vcc, exec, s[30:31]
	v_cvt_pk_bf16_f32 v135, v136, v135
	ds_write_b128 v185, v[132:135]
	s_cbranch_vccnz .LBB0_558
	s_cmp_ge_i32 s33, s101
	s_cbranch_scc1 .LBB0_557
	s_cmp_gt_i32 s33, 0xffff
	s_mov_b64 s[2:3], -1
	s_cbranch_scc0 .LBB0_554
	s_lshl_b32 s3, s33, 16
	s_add_i32 s2, s33, 0xffff0000
	s_and_b32 s3, s3, 0x3f0000
	s_lshr_b32 s2, s2, 10
	v_or_b32_e32 v132, s3, v160
	s_mov_b32 s3, s79
	s_lshl_b64 s[2:3], s[2:3], 22
	v_readlane_b32 s30, v255, 18
	s_add_u32 s2, s30, s2
	v_readlane_b32 s30, v255, 19
	v_mov_b32_e32 v133, v141
	s_addc_u32 s3, s30, s3
	v_lshl_add_u64 v[132:133], s[2:3], 0, v[132:133]
	s_lshl_b32 s30, s33, 1
	s_mov_b64 s[2:3], 0

; __device__ __forceinline__ void mlstm_unit(LAS unsigned char* lds, const bf16_t* __restrict__ PM, const float* __restrict__ GATES, bf16_t* __restrict__ Hout,
;                                            int b, int h, int dir, int vs, Conv& cvs, const int wave_) {
;     ...
;         if (ci + 1 < 36) ML_LOAD(ci + 1);
;         CV_ISSUE();
.LBB0_567:
	s_cmp_lt_i32 s33, s101
	s_cselect_b64 s[92:93], -1, 0
	s_cmp_ge_i32 s33, s101
	s_cbranch_scc1 .LBB0_574
	s_cmp_gt_i32 s33, 0xffff
	s_mov_b64 s[2:3], -1
	s_cbranch_scc0 .LBB0_570
	s_add_i32 s2, s33, 0xffff0000
	s_lshr_b32 s2, s2, 10
	s_mov_b32 s3, s79
	v_readlane_b32 s40, v254, 34
	s_lshl_b64 s[2:3], s[2:3], 24
	v_readlane_b32 s48, v254, 42
	v_readlane_b32 s49, v254, 43
	s_add_u32 s72, s48, s2
	v_readlane_b32 s41, v254, 35
	v_readlane_b32 s42, v254, 36
	v_readlane_b32 s43, v254, 37
	v_readlane_b32 s44, v254, 38
	v_readlane_b32 s45, v254, 39
	v_readlane_b32 s46, v254, 40
	v_readlane_b32 s47, v254, 41
	v_readlane_b32 s50, v254, 44
	v_readlane_b32 s51, v254, 45
	v_readlane_b32 s52, v254, 46
	v_readlane_b32 s53, v254, 47
	v_readlane_b32 s54, v254, 48
	v_readlane_b32 s55, v254, 49
	s_addc_u32 s73, s49, s3
	s_lshl_b32 s37, s33, 1
	s_mov_b64 s[2:3], 0

; __device__ __forceinline__ void mlstm_unit(LAS unsigned char* lds, const bf16_t* __restrict__ PM, const float* __restrict__ GATES, bf16_t* __restrict__ Hout,
;                                            int b, int h, int dir, int vs, Conv& cvs, const int wave_) {
;     ...
;         CV_FINISH();
;         if ((ci % 3) == 0) { CV_ISSUE(); pend_b = true; }
.LBB0_608:
	s_add_i32 s33, s33, s62
	s_mul_i32 s0, s0, 0xaaaaaaab
	s_cmp_lt_u32 s0, 0x55555556
	s_cselect_b64 s[30:31], -1, 0
	s_cmp_lt_i32 s33, s101
	s_cselect_b64 s[2:3], -1, 0
	s_and_b64 s[2:3], s[30:31], s[2:3]
	s_andn2_b64 vcc, exec, s[2:3]
	s_cbranch_vccnz .LBB0_615
	s_cmp_gt_i32 s33, 0xffff
	s_mov_b64 s[2:3], -1
	s_cbranch_scc0 .LBB0_611
	s_add_i32 s0, s33, 0xffff0000
	s_lshr_b32 s2, s0, 10
	s_mov_b32 s3, s79
	v_readlane_b32 s36, v254, 34
	s_lshl_b64 s[2:3], s[2:3], 24
	v_readlane_b32 s44, v254, 42
	v_readlane_b32 s45, v254, 43
	s_add_u32 s72, s44, s2
	v_readlane_b32 s37, v254, 35
	v_readlane_b32 s38, v254, 36
	v_readlane_b32 s39, v254, 37
	v_readlane_b32 s40, v254, 38
	v_readlane_b32 s41, v254, 39
	v_readlane_b32 s42, v254, 40
	v_readlane_b32 s43, v254, 41
	v_readlane_b32 s46, v254, 44
	v_readlane_b32 s47, v254, 45
	v_readlane_b32 s48, v254, 46
	v_readlane_b32 s49, v254, 47
	v_readlane_b32 s50, v254, 48
	v_readlane_b32 s51, v254, 49
	s_addc_u32 s73, s45, s3
	s_lshl_b32 s0, s33, 1
	s_mov_b64 s[2:3], 0

; __global__ void __launch_bounds__(NTHREADS, 2) fwd(Args args) {
;     ...
;                 f32x4 cv[16];
; #pragma unroll 1
;                 while (cvs.t < ml::T_CONV) { CV_ISSUE(); CV_FINISH(); }
.LBB0_624:
	s_cmp_ge_i32 s33, s101
	s_cbranch_scc1 .LBB0_636
	s_waitcnt vmcnt(0)
	v_lshlrev_b32_e32 v0, 1, v180
	v_and_b32_e32 v64, -16, v0
	v_lshlrev_b32_e32 v0, 2, v180
	v_and_b32_e32 v66, 28, v0
	v_mov_b32_e32 v69, 0
	v_lshlrev_b32_e32 v0, 13, v180
	v_and_b32_e32 v67, 0xe000, v0
	v_ashrrev_i32_e32 v65, 31, v64
	s_lshl_b32 s0, s33, 5
	s_lshl_b32 s1, s73, 8
	s_lshl_b32 s36, s33, 16
	s_lshl_b32 s37, s73, 19
	s_lshl_b32 s38, s33, 6
	s_lshl_b32 s39, s73, 9
	s_mov_b32 s3, 0
	v_lshlrev_b32_e32 v70, 2, v66
	v_mov_b32_e32 v71, v69
	s_branch .LBB0_627
.LBB0_626:
	s_waitcnt vmcnt(0)
	v_mul_f32_e32 v12, 0x42000000, v12
	v_mul_f32_e32 v8, 0x42000000, v8
	v_mov_b32_e32 v77, 0
	v_cvt_pk_fp8_f32 v77, v12, v8
	v_mul_f32_e32 v4, 0x42000000, v4
	v_mul_f32_e32 v0, 0x42000000, v0
	v_mov_b32_e32 v78, 0
	v_cvt_pk_fp8_f32 v77, v4, v0 op_sel:[0,0,1]
	v_mul_f32_e32 v0, 0x42000000, v61
	v_mul_f32_e32 v4, 0x42000000, v57
	v_cvt_pk_fp8_f32 v78, v0, v4
	v_mul_f32_e32 v0, 0x42000000, v45
	v_mul_f32_e32 v4, 0x42000000, v41
	v_mov_b32_e32 v79, 0
	v_cvt_pk_fp8_f32 v79, v0, v4
	v_mul_f32_e32 v0, 0x42000000, v37
	v_mul_f32_e32 v4, 0x42000000, v33
	v_mov_b32_e32 v80, 0
	v_cvt_pk_fp8_f32 v79, v0, v4 op_sel:[0,0,1]
	v_mul_f32_e32 v0, 0x42000000, v29
	v_mul_f32_e32 v4, 0x42000000, v25
	v_cvt_pk_fp8_f32 v80, v0, v4
	v_mul_f32_e32 v0, 0x42000000, v13
	v_mul_f32_e32 v4, 0x42000000, v9
	v_mov_b32_e32 v81, 0
	v_cvt_pk_fp8_f32 v81, v0, v4
	v_mul_f32_e32 v60, 0x42000000, v60
	v_mul_f32_e32 v56, 0x42000000, v56
	v_mov_b32_e32 v74, 0
	v_mul_f32_e32 v44, 0x42000000, v44
	v_mul_f32_e32 v40, 0x42000000, v40
	v_mov_b32_e32 v75, 0
	v_mul_f32_e32 v28, 0x42000000, v28
	v_mul_f32_e32 v24, 0x42000000, v24
	v_mov_b32_e32 v76, 0
	v_cvt_pk_fp8_f32 v74, v60, v56
	v_cvt_pk_fp8_f32 v75, v44, v40
	v_cvt_pk_fp8_f32 v76, v28, v24
	s_and_b32 s2, s2, 0x780
	v_mul_f32_e32 v0, 0x42000000, v5
	v_mul_f32_e32 v1, 0x42000000, v1
	v_cvt_pk_fp8_f32 v81, v0, v1 op_sel:[0,0,1]
	v_lshl_add_u64 v[0:1], v[72:73], 0, s[2:3]
	v_mul_f32_e32 v4, 0x42000000, v62
	v_mul_f32_e32 v5, 0x42000000, v58
	v_mov_b32_e32 v72, 0
	v_mul_f32_e32 v52, 0x42000000, v52
	v_mul_f32_e32 v48, 0x42000000, v48
	v_mul_f32_e32 v36, 0x42000000, v36
	v_mul_f32_e32 v32, 0x42000000, v32
	v_mul_f32_e32 v20, 0x42000000, v20
	v_mul_f32_e32 v16, 0x42000000, v16
	v_mul_f32_e32 v8, 0x42000000, v53
	v_mul_f32_e32 v12, 0x42000000, v49
	v_cvt_pk_fp8_f32 v72, v4, v5
	v_mul_f32_e32 v4, 0x42000000, v46
	v_mul_f32_e32 v5, 0x42000000, v42
	v_mov_b32_e32 v73, 0
	v_cvt_pk_fp8_f32 v74, v52, v48 op_sel:[0,0,1]
	v_cvt_pk_fp8_f32 v75, v36, v32 op_sel:[0,0,1]
	v_cvt_pk_fp8_f32 v76, v20, v16 op_sel:[0,0,1]
	v_cvt_pk_fp8_f32 v78, v8, v12 op_sel:[0,0,1]
	v_mul_f32_e32 v8, 0x42000000, v21
	v_mul_f32_e32 v12, 0x42000000, v17
	v_cvt_pk_fp8_f32 v73, v4, v5
	v_cvt_pk_fp8_f32 v80, v8, v12 op_sel:[0,0,1]
	v_lshl_add_u64 v[0:1], v[0:1], 0, v[64:65]
	v_mul_f32_e32 v4, 0x42000000, v38
	v_mul_f32_e32 v5, 0x42000000, v34
	global_store_dwordx4 v[0:1], v[74:77], off
	global_store_dwordx4 v[0:1], v[78:81], off offset:2048
	v_cvt_pk_fp8_f32 v73, v4, v5 op_sel:[0,0,1]
	v_mul_f32_e32 v4, 0x42000000, v30
	v_mul_f32_e32 v5, 0x42000000, v26
	v_mov_b32_e32 v74, 0
	v_cvt_pk_fp8_f32 v74, v4, v5
	v_mul_f32_e32 v4, 0x42000000, v14
	v_mul_f32_e32 v5, 0x42000000, v10
	v_mov_b32_e32 v75, 0
	v_cvt_pk_fp8_f32 v75, v4, v5
	v_mul_f32_e32 v8, 0x42000000, v54
	v_mul_f32_e32 v9, 0x42000000, v50
	v_cvt_pk_fp8_f32 v72, v8, v9 op_sel:[0,0,1]
	v_mul_f32_e32 v8, 0x42000000, v22
	v_mul_f32_e32 v9, 0x42000000, v18
	v_mul_f32_e32 v4, 0x42000000, v6
	v_mul_f32_e32 v2, 0x42000000, v2
	v_cvt_pk_fp8_f32 v74, v8, v9 op_sel:[0,0,1]
	v_cvt_pk_fp8_f32 v75, v4, v2 op_sel:[0,0,1]
	v_mul_f32_e32 v2, 0x42000000, v63
	v_mul_f32_e32 v4, 0x42000000, v59
	v_mov_b32_e32 v8, 0
	v_cvt_pk_fp8_f32 v8, v2, v4
	v_mul_f32_e32 v2, 0x42000000, v47
	v_mul_f32_e32 v4, 0x42000000, v43
	v_mov_b32_e32 v9, 0
	v_cvt_pk_fp8_f32 v9, v2, v4
	v_mul_f32_e32 v2, 0x42000000, v39
	v_mul_f32_e32 v4, 0x42000000, v35
	v_mov_b32_e32 v10, 0
	v_cvt_pk_fp8_f32 v9, v2, v4 op_sel:[0,0,1]
	v_mul_f32_e32 v2, 0x42000000, v31
	v_mul_f32_e32 v4, 0x42000000, v27
	v_cvt_pk_fp8_f32 v10, v2, v4
	v_mul_f32_e32 v2, 0x42000000, v15
	v_mul_f32_e32 v4, 0x42000000, v11
	v_mov_b32_e32 v11, 0
	v_cvt_pk_fp8_f32 v11, v2, v4
	v_mul_f32_e32 v5, 0x42000000, v55
	v_mul_f32_e32 v6, 0x42000000, v51
	v_cvt_pk_fp8_f32 v8, v5, v6 op_sel:[0,0,1]
	v_mul_f32_e32 v5, 0x42000000, v23
	v_mul_f32_e32 v6, 0x42000000, v19
	v_mul_f32_e32 v2, 0x42000000, v7
	v_mul_f32_e32 v3, 0x42000000, v3
	v_cvt_pk_fp8_f32 v10, v5, v6 op_sel:[0,0,1]
	v_cvt_pk_fp8_f32 v11, v2, v3 op_sel:[0,0,1]
	s_movk_i32 s2, 0x1000
	v_add_co_u32_e32 v0, vcc, s2, v0
	s_add_i32 s33, s33, s62
	s_add_i32 s0, s0, s1
	s_add_i32 s36, s36, s37
	s_add_i32 s38, s38, s39
	v_addc_co_u32_e32 v1, vcc, 0, v1, vcc
	s_cmp_lt_i32 s33, s101
	global_store_dwordx4 v[0:1], v[72:75], off
	global_store_dwordx4 v[0:1], v[8:11], off offset:2048
	s_cbranch_scc0 .LBB0_636

; __device__ __forceinline__ int lane_id_() { int l; asm volatile("v_mbcnt_lo_u32_b32 %0, -1, 0\n\tv_mbcnt_hi_u32_b32 %0, -1, %0" : "=v"(l)); return l; }
; __device__ __forceinline__ unsigned xb_add(unsigned* p, unsigned v) { return __hip_atomic_fetch_add(p, v, __ATOMIC_RELAXED, __HIP_MEMORY_SCOPE_AGENT); }
; #define SEAM(k) do { if (IN(k) && IN((k) + 1)) xcd_barrier(bar, wave); } while (0)
; __device__ __forceinline__ void xcd_barrier(const XcdBarrier& b, int wave_) {
;     asm volatile("s_waitcnt vmcnt(0)" ::: "memory");
;     __syncthreads();
;     if (wave_ == 0 && lane_id_() == 0) {
;         unsigned* bar = b.bar;
;         __builtin_amdgcn_s_waitcnt(0);
;         unsigned nloc = b.st[0], nx = b.st[1];
;         if (nloc == 0u) { xcd_barrier_complete(bar, b.x, nloc, nx); b.st[0] = nloc; b.st[1] = nx; }
;         const unsigned old = xb_add(&bar[XB_XSUB(b.x)], 1u);
; __global__ void __launch_bounds__(NTHREADS, 2) fwd(Args args) {
;     ...
;         __syncthreads();
;         if (!att_first) { ATT_BLOCK(); }
;     ...
;     }
;     SEAM(4);
.LBB0_636:
	v_readlane_b32 s0, v255, 26
	v_readlane_b32 s1, v255, 27
	s_and_b64 vcc, exec, s[0:1]
	v_readlane_b32 s57, v255, 28
	s_waitcnt vmcnt(0) lgkmcnt(0)
	s_barrier
	s_cbranch_vccz .LBB0_659
	s_branch .Latt1_entry
.LBB0_659:
	s_mov_b32 s99, 0
	s_cmp_gt_i32 s97, 5
	v_readlane_b32 s0, v255, 21
	s_cselect_b64 s[2:3], -1, 0
	v_readlane_b32 s1, v255, 22
	s_and_b64 s[0:1], s[0:1], s[2:3]
	v_readlane_b32 s74, v254, 58
	v_readlane_b32 s58, v255, 8
	s_andn2_b64 vcc, exec, s[0:1]
	v_readlane_b32 s75, v254, 59
	v_readlane_b32 s33, v254, 51
	v_readlane_b32 s64, v254, 57
	v_readlane_b32 s65, v254, 56
	v_readlane_b32 s55, v254, 55
	v_readlane_b32 s56, v254, 54
	v_readlane_b32 s59, v255, 9
	v_readlane_b32 s34, v255, 2
	v_readlane_b32 s35, v255, 3
	v_readlane_b32 s60, v255, 20
	s_cbranch_vccnz .LBB0_715
	s_waitcnt vmcnt(0)
	v_readlane_b32 s0, v254, 52
	v_readlane_b32 s1, v254, 53
	s_and_b64 vcc, exec, s[0:1]
	s_waitcnt vmcnt(0) lgkmcnt(0)
	s_barrier
	s_cbranch_vccnz .LBB0_714
	v_mbcnt_lo_u32_b32 v0, -1, 0
	v_mbcnt_hi_u32_b32 v0, -1, v0
	s_nop 0
	v_cmp_eq_u32_e32 vcc, 0, v0
	s_and_saveexec_b64 s[4:5], vcc
	s_cbranch_execz .LBB0_713
	s_add_i32 s0, 0, 0x21c00
	v_mov_b32_e32 v0, s0
	s_waitcnt vmcnt(0) expcnt(0) lgkmcnt(0)
	ds_read_b32 v2, v0
	s_add_i32 s0, 0, 0x21c04
	v_mov_b32_e32 v0, s0
	ds_read_b32 v0, v0
	s_waitcnt lgkmcnt(1)
	v_cmp_ne_u32_e32 vcc, 0, v2
	s_cbranch_vccnz .LBB0_677
	v_readlane_b32 s6, v254, 0
	v_readlane_b32 s8, v254, 34
	v_readlane_b32 s7, v254, 1
	v_readlane_b32 s22, v254, 48
	s_load_dwordx2 s[0:1], s[6:7], 0x4
	v_readlane_b32 s23, v254, 49
	s_add_u32 s6, s22, 0x1000
	s_addc_u32 s7, s23, 0
	v_readlane_b32 s9, v254, 35
	s_add_u32 s8, s22, 0x1100
	v_readlane_b32 s10, v254, 36
	s_addc_u32 s9, s23, 0
	v_readlane_b32 s11, v254, 37
	s_add_u32 s10, s22, 0x1200
	v_readlane_b32 s12, v254, 38
	s_addc_u32 s11, s23, 0
	v_readlane_b32 s13, v254, 39
	s_waitcnt lgkmcnt(0)
	s_mul_i32 s0, s0, s73
	s_add_u32 s12, s22, 0x1300
	s_mul_i32 s0, s0, s1
	s_addc_u32 s13, s23, 0
	s_mov_b32 s1, 1
	v_mov_b32_e32 v16, 0
	v_readlane_b32 s14, v254, 40
	v_readlane_b32 s15, v254, 41
	v_readlane_b32 s16, v254, 42
	v_readlane_b32 s17, v254, 43
	v_readlane_b32 s18, v254, 44
	v_readlane_b32 s19, v254, 45
	v_readlane_b32 s20, v254, 46
	v_readlane_b32 s21, v254, 47
	s_branch .LBB0_665

; template <class Epi, class Sched, class Ops, bool FP8 = false>
; __device__ __forceinline__ void gemm_phase(LAS unsigned char* lds, const int RB, const Sched& S, const Ops& G, const Epi& E, const int wave_) {
;     ...
;         if constexpr (FP8) {
;             asm volatile("s_nop 15\n\ts_nop 15" ::: "memory");
; #pragma unroll
;             for (int a = 0; a < 2; ++a)
; #pragma unroll
;                 for (int b = 0; b < 2; ++b)
; #pragma unroll
;                     for (int m = 0; m < 4; ++m) asm volatile("" : "+v"(acc[a][b][m][0]), "+v"(acc[a][b][m][1]));
;         }
;         E(acc, cur, wr, wc, fr, fq);
;     __device__ __forceinline__ void operator()(const g8::Acc& acc, const g8::Unit& u, int wr, int wc, int fr, int fq) const {
;         const int row0 = u.pm * 256 + wr * 64 + fr, j0 = u.pn * 128 + wc * 32 + 8 * fq;
;         const float* bg = bgu + (size_t)u.e * 4096 + j0; const float* bu = bg + 2048;
;         const f32x4 g0 = *(const f32x4*)bg, g1 = *(const f32x4*)(bg + 4), u0 = *(const f32x4*)bu, u1 = *(const f32x4*)(bu + 4);
.LBB0_1178:
	s_nop 15
	s_nop 15
	s_and_b64 vcc, exec, s[8:9]
	s_cbranch_vccz .LBB0_1139
	v_ashrrev_i32_e32 v197, 31, v196
	v_readlane_b32 s80, v254, 34
	v_lshl_add_u32 v220, s58, 7, v231
	v_lshlrev_b64 v[66:67], 14, v[196:197]
	v_readlane_b32 s86, v254, 40
	v_readlane_b32 s87, v254, 41
	v_ashrrev_i32_e32 v221, 31, v220
	v_lshl_add_u32 v222, s78, 8, v230
	v_lshl_add_u64 v[66:67], s[86:87], 0, v[66:67]
	v_lshl_add_u64 v[66:67], v[220:221], 2, v[66:67]
	global_load_dwordx4 v[208:211], v[66:67], off
	global_load_dwordx4 v[200:203], v[66:67], off offset:16
	v_add_co_u32_e32 v196, vcc, 0x2000, v66
	v_readlane_b32 s81, v254, 35
	s_nop 0
	v_addc_co_u32_e32 v197, vcc, 0, v67, vcc
	v_lshl_add_u64 v[66:67], v[66:67], 0, s[52:53]
	global_load_dwordx4 v[204:207], v[196:197], off
	s_and_b64 vcc, exec, s[4:5]
	global_load_dwordx4 v[196:199], v[66:67], off offset:16
	v_readlane_b32 s82, v254, 36
	v_readlane_b32 s83, v254, 37
	v_readlane_b32 s84, v254, 38
	v_readlane_b32 s85, v254, 39
	v_readlane_b32 s88, v254, 42
	v_readlane_b32 s89, v254, 43
	v_readlane_b32 s90, v254, 44
	v_readlane_b32 s91, v254, 45
	v_readlane_b32 s92, v254, 46
	v_readlane_b32 s93, v254, 47
	v_readlane_b32 s94, v254, 48
	v_readlane_b32 s95, v254, 49
	s_mov_b32 s99, 0
	s_cmp_lt_u32 s98, 0x18000
	s_cbranch_scc0 .Lp9e_noissue
	s_mov_b32 s99, s98
	v_mbcnt_lo_u32_b32 v244, -1, 0
	v_mbcnt_hi_u32_b32 v244, -1, v244
	s_sub_i32 s100, s99, 0x10000
	s_lshr_b32 s100, s100, 10
	s_lshl_b32 s100, s100, 24
	s_bfe_u32 s101, s99, 0x40006
	s_lshl_b32 s101, s101, 20
	s_add_i32 s100, s100, s101
	s_and_b32 s101, s99, 63
	s_lshl_b32 s101, s101, 7
	s_add_i32 s100, s100, s101
	v_lshrrev_b32_e32 v245, 3, v244
	v_and_b32_e32 v246, 7, v244
	v_lshlrev_b32_e32 v245, 17, v245
	v_lshl_or_b32 v245, v246, 4, v245
	v_add_u32_e32 v245, s100, v245
	v_readlane_b32 s100, v254, 42
	v_readlane_b32 s101, v254, 43
	s_nop 4
	global_load_dwordx4 v[0:3], v245, s[100:101] nt
	v_add_u32_e32 v245, 0x2000, v245
	global_load_dwordx4 v[4:7], v245, s[100:101] nt
	v_add_u32_e32 v245, 0x2000, v245
	global_load_dwordx4 v[8:11], v245, s[100:101] nt
	v_add_u32_e32 v245, 0x2000, v245
	global_load_dwordx4 v[12:15], v245, s[100:101] nt
	v_add_u32_e32 v245, 0x2000, v245
	global_load_dwordx4 v[16:19], v245, s[100:101] nt
	v_add_u32_e32 v245, 0x2000, v245
	global_load_dwordx4 v[20:23], v245, s[100:101] nt
	v_add_u32_e32 v245, 0x2000, v245
	global_load_dwordx4 v[24:27], v245, s[100:101] nt
	v_add_u32_e32 v245, 0x2000, v245
	global_load_dwordx4 v[28:31], v245, s[100:101] nt
	v_add_u32_e32 v245, 0x2000, v245
	global_load_dwordx4 v[32:35], v245, s[100:101] nt
	v_add_u32_e32 v245, 0x2000, v245
	global_load_dwordx4 v[36:39], v245, s[100:101] nt
	v_add_u32_e32 v245, 0x2000, v245
	global_load_dwordx4 v[40:43], v245, s[100:101] nt
	v_add_u32_e32 v245, 0x2000, v245
	global_load_dwordx4 v[44:47], v245, s[100:101] nt
	v_add_u32_e32 v245, 0x2000, v245
	global_load_dwordx4 v[48:51], v245, s[100:101] nt
	v_add_u32_e32 v245, 0x2000, v245
	global_load_dwordx4 v[52:55], v245, s[100:101] nt
	v_add_u32_e32 v245, 0x2000, v245
	global_load_dwordx4 v[56:59], v245, s[100:101] nt
	v_add_u32_e32 v245, 0x2000, v245
	global_load_dwordx4 v[60:63], v245, s[100:101] nt
	s_waitcnt vmcnt(16)
	s_branch .Lp9e_joined

; __device__ __forceinline__ float sigmoidf_(float x) { return __builtin_amdgcn_rcpf(1.f + __expf(-x)); }
;     __device__ __forceinline__ void operator()(const g8::Acc& acc, const g8::Unit& u, int wr, int wc, int fr, int fq) const {
;     ...
; #pragma unroll
;         for (int ai = 0; ai < 2; ++ai) {
;             if (u.hm <= ai * 128 + wr * 64) break;
; #pragma unroll
;             for (int m = 0; m < 4; ++m) {
;                 f32x4 ga = acc[ai][0][m][0] * WINV + g0, gb = acc[ai][0][m][1] * WINV + g1, ua = acc[ai][1][m][0] * WINV + u0, ub = acc[ai][1][m][1] * WINV + u1;
;                 f32x4 ha, hb;
; #pragma unroll
;                 for (int j = 0; j < 4; ++j) {
;                     const float gt = fminf(ga[j], 7.f), up = fminf(fmaxf(ua[j], -7.f), 7.f);
;                     ha[j] = (up + 1.f) * gt * sigmoidf_(1.702f * gt);
;                     const float gt2 = fminf(gb[j], 7.f), up2 = fminf(fmaxf(ub[j], -7.f), 7.f);
;                     hb[j] = (up2 + 1.f) * gt2 * sigmoidf_(1.702f * gt2);
;                 }
;                 u32x2 w; w.x = pk4_fp8s(ha[0], ha[1], ha[2], ha[3]); w.y = pk4_fp8s(hb[0], hb[1], hb[2], hb[3]);
;                 *(u32x2*)(HID + (size_t)(row0 + ai * 128 + m * 16) * 2048 + j0) = w;
;             }
.Lp9e_joined:
	v_fmamk_f32 v67, v193, 0x3d000000, v209
	v_fmamk_f32 v66, v184, 0x3d000000, v200
	v_min_f32_e32 v66, 0x40e00000, v66
	v_fmamk_f32 v184, v185, 0x3d000000, v201
	v_fmamk_f32 v185, v194, 0x3d000000, v210
	v_mul_f32_e32 v194, 0x3fd9db23, v66
	v_min_f32_e32 v67, 0x40e00000, v67
	v_mul_f32_e32 v194, 0xbfb8aa3b, v194
	v_fmamk_f32 v64, v192, 0x3d000000, v208
	v_fmamk_f32 v192, v195, 0x3d000000, v211
	v_mul_f32_e32 v195, 0x3fd9db23, v67
	v_exp_f32_e32 v194, v194
	v_fmamk_f32 v180, v180, 0x3d000000, v196
	v_fmamk_f32 v181, v181, 0x3d000000, v197
	v_fmamk_f32 v190, v190, 0x3d000000, v206
	v_mul_f32_e32 v195, 0xbfb8aa3b, v195
	v_med3_f32 v180, v180, s71, v235
	v_med3_f32 v181, v181, s71, v235
	v_med3_f32 v190, v190, s71, v235
	v_exp_f32_e32 v195, v195
	v_min_f32_e32 v184, 0x40e00000, v184
	v_min_f32_e32 v185, 0x40e00000, v185
	v_fmamk_f32 v182, v182, 0x3d000000, v198
	v_add_f32_e32 v180, 1.0, v180
	v_add_f32_e32 v181, 1.0, v181
	v_add_f32_e32 v190, 1.0, v190
	v_fmamk_f32 v186, v186, 0x3d000000, v202
	v_mul_f32_e32 v241, 0x3fd9db23, v185
	v_med3_f32 v182, v182, s71, v235
	v_mul_f32_e32 v66, v66, v180
	v_mul_f32_e32 v180, v184, v181
	v_mul_f32_e32 v181, v185, v190
	v_add_f32_e32 v185, 1.0, v194
	v_min_f32_e32 v64, 0x40e00000, v64
	v_min_f32_e32 v186, 0x40e00000, v186
	v_add_f32_e32 v182, 1.0, v182
	v_rcp_f32_e32 v185, v185
	v_mul_f32_e32 v193, 0x3fd9db23, v64
	v_mul_f32_e32 v223, 0x3fd9db23, v184
	v_mul_f32_e32 v242, 0x3fd9db23, v186
	v_mul_f32_e32 v182, v186, v182
	v_add_f32_e32 v186, 1.0, v195
	v_fmamk_f32 v189, v189, 0x3d000000, v205
	v_mul_f32_e32 v193, 0xbfb8aa3b, v193
	v_mul_f32_e32 v223, 0xbfb8aa3b, v223
	v_mul_f32_e32 v241, 0xbfb8aa3b, v241
	v_rcp_f32_e32 v186, v186
	v_med3_f32 v189, v189, s71, v235
	v_exp_f32_e32 v193, v193
	v_exp_f32_e32 v223, v223
	v_exp_f32_e32 v241, v241
	v_min_f32_e32 v192, 0x40e00000, v192
	v_fmamk_f32 v188, v188, 0x3d000000, v204
	v_add_f32_e32 v189, 1.0, v189
	v_mul_f32_e32 v66, v66, v185
	v_fmamk_f32 v185, v187, 0x3d000000, v203
	v_mul_f32_e32 v243, 0x3fd9db23, v192
	v_med3_f32 v188, v188, s71, v235
	v_mul_f32_e32 v67, v67, v189
	v_min_f32_e32 v185, 0x40e00000, v185
	v_mul_f32_e32 v243, 0xbfb8aa3b, v243
	v_add_f32_e32 v188, 1.0, v188
	v_mul_f32_e32 v67, v67, v186
	v_mul_f32_e32 v186, 0x3fd9db23, v185
	v_exp_f32_e32 v243, v243
	v_mul_f32_e32 v64, v64, v188
	v_add_f32_e32 v184, 1.0, v193
	v_add_f32_e32 v188, 1.0, v223
	v_add_f32_e32 v189, 1.0, v241
	v_mul_f32_e32 v186, 0xbfb8aa3b, v186
	v_rcp_f32_e32 v184, v184
	v_rcp_f32_e32 v188, v188
	v_rcp_f32_e32 v189, v189
	v_exp_f32_e32 v186, v186
	v_mul_f32_e32 v242, 0xbfb8aa3b, v242
	v_exp_f32_e32 v242, v242
	v_add_f32_e32 v193, 1.0, v243
	v_fmamk_f32 v191, v191, 0x3d000000, v207
	v_mul_f32_e32 v64, v64, v184
	v_mul_f32_e32 v184, v180, v188
	v_mul_f32_e32 v180, v181, v189
	v_rcp_f32_e32 v181, v193
	v_add_f32_e32 v186, 1.0, v186
	v_med3_f32 v191, v191, s71, v235
	v_fmamk_f32 v183, v183, 0x3d000000, v199
	v_rcp_f32_e32 v186, v186
	v_add_f32_e32 v191, 1.0, v191
	v_med3_f32 v183, v183, s71, v235
	v_add_f32_e32 v190, 1.0, v242
	v_mul_f32_e32 v187, v192, v191
	v_add_f32_e32 v183, 1.0, v183
	v_rcp_f32_e32 v190, v190
	v_mul_f32_e32 v181, v187, v181
	v_mul_f32_e32 v183, v185, v183
	v_med3_f32 v64, v64, s72, v236
	v_med3_f32 v67, v67, s72, v236
	v_med3_f32 v185, v180, s72, v236
	v_mov_b32_e32 v180, v65
	v_mul_f32_e32 v183, v183, v186
	v_med3_f32 v186, v181, s72, v236
	v_cvt_pk_fp8_f32 v180, v64, v67
	v_med3_f32 v64, v66, s72, v236
	v_med3_f32 v66, v184, s72, v236
	v_mov_b32_e32 v181, v65
	v_cvt_pk_fp8_f32 v181, v64, v66
	v_mul_f32_e32 v182, v182, v190
	v_med3_f32 v64, v182, s72, v236
	v_med3_f32 v66, v183, s72, v236
	v_cvt_pk_fp8_f32 v180, v185, v186 op_sel:[0,0,1]
	v_cvt_pk_fp8_f32 v181, v64, v66 op_sel:[0,0,1]
	v_ashrrev_i32_e32 v223, 31, v222
	v_lshlrev_b64 v[66:67], 11, v[222:223]
	v_lshl_add_u64 v[66:67], s[16:17], 0, v[66:67]
	v_fmamk_f32 v64, v176, 0x3d000000, v208
	v_fmamk_f32 v172, v172, 0x3d000000, v200
	v_lshl_add_u64 v[66:67], v[66:67], 0, v[220:221]
	v_min_f32_e32 v64, 0x40e00000, v64
	v_min_f32_e32 v172, 0x40e00000, v172
	global_store_dwordx2 v[66:67], v[180:181], off
	v_mul_f32_e32 v176, 0x3fd9db23, v64
	v_mul_f32_e32 v180, 0x3fd9db23, v172
	v_mul_f32_e32 v176, 0xbfb8aa3b, v176
	v_mul_f32_e32 v180, 0xbfb8aa3b, v180
	v_exp_f32_e32 v176, v176
	v_exp_f32_e32 v180, v180
	v_fmamk_f32 v168, v168, 0x3d000000, v204
	v_med3_f32 v168, v168, s71, v235
	v_add_f32_e32 v168, 1.0, v168
	v_add_f32_e32 v176, 1.0, v176
	v_mul_f32_e32 v64, v64, v168
	v_add_f32_e32 v168, 1.0, v180
	v_rcp_f32_e32 v176, v176
	v_fmamk_f32 v164, v164, 0x3d000000, v196
	v_rcp_f32_e32 v168, v168
	v_med3_f32 v164, v164, s71, v235
	v_add_f32_e32 v164, 1.0, v164
	v_fmamk_f32 v173, v173, 0x3d000000, v201
	v_mul_f32_e32 v164, v172, v164
	v_min_f32_e32 v173, 0x40e00000, v173
	v_mul_f32_e32 v64, v64, v176
	v_mul_f32_e32 v168, v164, v168
	v_fmamk_f32 v164, v177, 0x3d000000, v209
	v_mul_f32_e32 v176, 0x3fd9db23, v173
	v_min_f32_e32 v164, 0x40e00000, v164
	v_mul_f32_e32 v176, 0xbfb8aa3b, v176
	v_mul_f32_e32 v172, 0x3fd9db23, v164
	v_exp_f32_e32 v176, v176
	v_mul_f32_e32 v172, 0xbfb8aa3b, v172
	v_fmamk_f32 v169, v169, 0x3d000000, v205
	v_exp_f32_e32 v172, v172
	v_med3_f32 v169, v169, s71, v235
	v_add_f32_e32 v169, 1.0, v169
	v_mul_f32_e32 v164, v164, v169
	v_fmamk_f32 v165, v165, 0x3d000000, v197
	v_add_f32_e32 v169, 1.0, v176
	v_rcp_f32_e32 v169, v169
	v_med3_f32 v165, v165, s71, v235
	v_add_f32_e32 v172, 1.0, v172
	v_add_f32_e32 v165, 1.0, v165
	v_rcp_f32_e32 v172, v172
	v_mul_f32_e32 v165, v173, v165
	v_fmamk_f32 v173, v174, 0x3d000000, v202
	v_min_f32_e32 v173, 0x40e00000, v173
	v_mul_f32_e32 v165, v165, v169
; __device__ __forceinline__ float sigmoidf_(float x) { return __builtin_amdgcn_rcpf(1.f + __expf(-x)); }
;     __device__ __forceinline__ void operator()(const g8::Acc& acc, const g8::Unit& u, int wr, int wc, int fr, int fq) const {
;     ...
; #pragma unroll
;         for (int ai = 0; ai < 2; ++ai) {
;             if (u.hm <= ai * 128 + wr * 64) break;
; #pragma unroll
;             for (int m = 0; m < 4; ++m) {
;                 f32x4 ga = acc[ai][0][m][0] * WINV + g0, gb = acc[ai][0][m][1] * WINV + g1, ua = acc[ai][1][m][0] * WINV + u0, ub = acc[ai][1][m][1] * WINV + u1;
;                 f32x4 ha, hb;
; #pragma unroll
;                 for (int j = 0; j < 4; ++j) {
;                     const float gt = fminf(ga[j], 7.f), up = fminf(fmaxf(ua[j], -7.f), 7.f);
;                     ha[j] = (up + 1.f) * gt * sigmoidf_(1.702f * gt);
;                     const float gt2 = fminf(gb[j], 7.f), up2 = fminf(fmaxf(ub[j], -7.f), 7.f);
;                     hb[j] = (up2 + 1.f) * gt2 * sigmoidf_(1.702f * gt2);
;                 }
;                 u32x2 w; w.x = pk4_fp8s(ha[0], ha[1], ha[2], ha[3]); w.y = pk4_fp8s(hb[0], hb[1], hb[2], hb[3]);
;                 *(u32x2*)(HID + (size_t)(row0 + ai * 128 + m * 16) * 2048 + j0) = w;
;             }
	v_fmamk_f32 v169, v178, 0x3d000000, v210
	v_mul_f32_e32 v174, 0x3fd9db23, v173
	v_min_f32_e32 v169, 0x40e00000, v169
	v_mul_f32_e32 v174, 0xbfb8aa3b, v174
	v_mul_f32_e32 v164, v164, v172
	v_mul_f32_e32 v172, 0x3fd9db23, v169
	v_exp_f32_e32 v174, v174
	v_mul_f32_e32 v172, 0xbfb8aa3b, v172
	v_fmamk_f32 v170, v170, 0x3d000000, v206
	v_fmamk_f32 v166, v166, 0x3d000000, v198
	v_exp_f32_e32 v172, v172
	v_med3_f32 v170, v170, s71, v235
	v_med3_f32 v166, v166, s71, v235
	v_add_f32_e32 v170, 1.0, v170
	v_add_f32_e32 v166, 1.0, v166
	v_mul_f32_e32 v169, v169, v170
	v_add_f32_e32 v170, 1.0, v174
	v_mul_f32_e32 v166, v173, v166
	v_fmamk_f32 v173, v175, 0x3d000000, v203
	v_rcp_f32_e32 v170, v170
	v_min_f32_e32 v173, 0x40e00000, v173
	v_add_f32_e32 v172, 1.0, v172
	v_mul_f32_e32 v174, 0x3fd9db23, v173
	v_rcp_f32_e32 v172, v172
	v_mul_f32_e32 v174, 0xbfb8aa3b, v174
	v_exp_f32_e32 v174, v174
	v_mul_f32_e32 v166, v166, v170
	v_fmamk_f32 v170, v179, 0x3d000000, v211
	v_fmamk_f32 v171, v171, 0x3d000000, v207
	v_min_f32_e32 v170, 0x40e00000, v170
	v_med3_f32 v171, v171, s71, v235
	v_mul_f32_e32 v169, v169, v172
	v_mul_f32_e32 v172, 0x3fd9db23, v170
	v_add_f32_e32 v171, 1.0, v171
	v_mul_f32_e32 v172, 0xbfb8aa3b, v172
	v_mul_f32_e32 v170, v170, v171
	v_add_f32_e32 v171, 1.0, v174
	v_exp_f32_e32 v172, v172
	v_fmamk_f32 v167, v167, 0x3d000000, v199
	v_rcp_f32_e32 v171, v171
	v_med3_f32 v167, v167, s71, v235
	v_add_f32_e32 v167, 1.0, v167
	v_mul_f32_e32 v167, v173, v167
	v_add_f32_e32 v172, 1.0, v172
	v_mul_f32_e32 v167, v167, v171
	v_med3_f32 v64, v64, s72, v236
	v_med3_f32 v171, v164, s72, v236
	v_mov_b32_e32 v164, v65
	v_rcp_f32_e32 v172, v172
	v_cvt_pk_fp8_f32 v164, v64, v171
	v_med3_f32 v64, v168, s72, v236
	v_med3_f32 v168, v165, s72, v236
	v_mov_b32_e32 v165, v65
	v_cvt_pk_fp8_f32 v165, v64, v168
	v_mul_f32_e32 v170, v170, v172
	v_med3_f32 v64, v166, s72, v236
	v_med3_f32 v166, v167, s72, v236
	v_med3_f32 v169, v169, s72, v236
	v_med3_f32 v170, v170, s72, v236
	v_cvt_pk_fp8_f32 v165, v64, v166 op_sel:[0,0,1]
	v_or_b32_e32 v166, 16, v222
	v_cvt_pk_fp8_f32 v164, v169, v170 op_sel:[0,0,1]
	v_ashrrev_i32_e32 v167, 31, v166
	v_lshlrev_b64 v[166:167], 11, v[166:167]
	v_lshl_add_u64 v[166:167], s[16:17], 0, v[166:167]
	v_fmamk_f32 v64, v160, 0x3d000000, v208
	v_fmamk_f32 v156, v156, 0x3d000000, v200
	v_lshl_add_u64 v[166:167], v[166:167], 0, v[220:221]
	v_min_f32_e32 v64, 0x40e00000, v64
	v_min_f32_e32 v156, 0x40e00000, v156
	global_store_dwordx2 v[166:167], v[164:165], off
	v_mul_f32_e32 v160, 0x3fd9db23, v64
	v_mul_f32_e32 v164, 0x3fd9db23, v156
	v_mul_f32_e32 v160, 0xbfb8aa3b, v160
	v_mul_f32_e32 v164, 0xbfb8aa3b, v164
	v_exp_f32_e32 v160, v160
	v_exp_f32_e32 v164, v164
	v_fmamk_f32 v152, v152, 0x3d000000, v204
	v_med3_f32 v152, v152, s71, v235
	v_add_f32_e32 v152, 1.0, v152
	v_add_f32_e32 v160, 1.0, v160
	v_mul_f32_e32 v64, v64, v152
	v_add_f32_e32 v152, 1.0, v164
	v_rcp_f32_e32 v160, v160
	v_fmamk_f32 v148, v148, 0x3d000000, v196
	v_rcp_f32_e32 v152, v152
	v_med3_f32 v148, v148, s71, v235
	v_add_f32_e32 v148, 1.0, v148
	v_fmamk_f32 v157, v157, 0x3d000000, v201
	v_mul_f32_e32 v148, v156, v148
	v_min_f32_e32 v157, 0x40e00000, v157
	v_mul_f32_e32 v64, v64, v160
	v_mul_f32_e32 v152, v148, v152
	v_fmamk_f32 v148, v161, 0x3d000000, v209
	v_mul_f32_e32 v160, 0x3fd9db23, v157
	v_min_f32_e32 v148, 0x40e00000, v148
	v_mul_f32_e32 v160, 0xbfb8aa3b, v160
	v_mul_f32_e32 v156, 0x3fd9db23, v148
	v_exp_f32_e32 v160, v160
	v_mul_f32_e32 v156, 0xbfb8aa3b, v156
	v_fmamk_f32 v153, v153, 0x3d000000, v205
	v_exp_f32_e32 v156, v156
	v_med3_f32 v153, v153, s71, v235
	v_add_f32_e32 v153, 1.0, v153
	v_mul_f32_e32 v148, v148, v153
	v_fmamk_f32 v149, v149, 0x3d000000, v197
	v_add_f32_e32 v153, 1.0, v160
	v_rcp_f32_e32 v153, v153
	v_med3_f32 v149, v149, s71, v235
	v_add_f32_e32 v156, 1.0, v156
	v_add_f32_e32 v149, 1.0, v149
	v_rcp_f32_e32 v156, v156
	v_mul_f32_e32 v149, v157, v149
	v_fmamk_f32 v157, v158, 0x3d000000, v202
	v_min_f32_e32 v157, 0x40e00000, v157
	v_mul_f32_e32 v149, v149, v153
	v_fmamk_f32 v153, v162, 0x3d000000, v210
	v_mul_f32_e32 v158, 0x3fd9db23, v157
	v_min_f32_e32 v153, 0x40e00000, v153
	v_mul_f32_e32 v158, 0xbfb8aa3b, v158
	v_mul_f32_e32 v148, v148, v156
	v_mul_f32_e32 v156, 0x3fd9db23, v153
	v_exp_f32_e32 v158, v158
	v_mul_f32_e32 v156, 0xbfb8aa3b, v156
	v_fmamk_f32 v154, v154, 0x3d000000, v206
	v_fmamk_f32 v150, v150, 0x3d000000, v198
	v_exp_f32_e32 v156, v156
	v_med3_f32 v154, v154, s71, v235
	v_med3_f32 v150, v150, s71, v235
	v_add_f32_e32 v154, 1.0, v154
	v_add_f32_e32 v150, 1.0, v150
	v_mul_f32_e32 v153, v153, v154
	v_add_f32_e32 v154, 1.0, v158
	v_mul_f32_e32 v150, v157, v150
	v_fmamk_f32 v157, v159, 0x3d000000, v203
	v_rcp_f32_e32 v154, v154
	v_min_f32_e32 v157, 0x40e00000, v157
	v_add_f32_e32 v156, 1.0, v156
	v_mul_f32_e32 v158, 0x3fd9db23, v157
	v_rcp_f32_e32 v156, v156
	v_mul_f32_e32 v158, 0xbfb8aa3b, v158
	v_exp_f32_e32 v158, v158
	v_mul_f32_e32 v150, v150, v154
	v_fmamk_f32 v154, v163, 0x3d000000, v211
	v_fmamk_f32 v155, v155, 0x3d000000, v207
	v_min_f32_e32 v154, 0x40e00000, v154
	v_med3_f32 v155, v155, s71, v235
	v_mul_f32_e32 v153, v153, v156
	v_mul_f32_e32 v156, 0x3fd9db23, v154
	v_add_f32_e32 v155, 1.0, v155
	v_mul_f32_e32 v156, 0xbfb8aa3b, v156
	v_mul_f32_e32 v154, v154, v155
	v_add_f32_e32 v155, 1.0, v158
	v_exp_f32_e32 v156, v156
	v_fmamk_f32 v151, v151, 0x3d000000, v199
	v_rcp_f32_e32 v155, v155
	v_med3_f32 v151, v151, s71, v235
	v_add_f32_e32 v151, 1.0, v151
	v_mul_f32_e32 v151, v157, v151
	v_add_f32_e32 v156, 1.0, v156
	v_mul_f32_e32 v151, v151, v155
	v_med3_f32 v64, v64, s72, v236
	v_med3_f32 v155, v148, s72, v236
	v_mov_b32_e32 v148, v65
; __device__ __forceinline__ float sigmoidf_(float x) { return __builtin_amdgcn_rcpf(1.f + __expf(-x)); }
;     __device__ __forceinline__ void operator()(const g8::Acc& acc, const g8::Unit& u, int wr, int wc, int fr, int fq) const {
;     ...
; #pragma unroll
;         for (int ai = 0; ai < 2; ++ai) {
;             if (u.hm <= ai * 128 + wr * 64) break;
; #pragma unroll
;             for (int m = 0; m < 4; ++m) {
;                 f32x4 ga = acc[ai][0][m][0] * WINV + g0, gb = acc[ai][0][m][1] * WINV + g1, ua = acc[ai][1][m][0] * WINV + u0, ub = acc[ai][1][m][1] * WINV + u1;
;                 f32x4 ha, hb;
; #pragma unroll
;                 for (int j = 0; j < 4; ++j) {
;                     const float gt = fminf(ga[j], 7.f), up = fminf(fmaxf(ua[j], -7.f), 7.f);
;                     ha[j] = (up + 1.f) * gt * sigmoidf_(1.702f * gt);
;                     const float gt2 = fminf(gb[j], 7.f), up2 = fminf(fmaxf(ub[j], -7.f), 7.f);
;                     hb[j] = (up2 + 1.f) * gt2 * sigmoidf_(1.702f * gt2);
;                 }
;                 u32x2 w; w.x = pk4_fp8s(ha[0], ha[1], ha[2], ha[3]); w.y = pk4_fp8s(hb[0], hb[1], hb[2], hb[3]);
;                 *(u32x2*)(HID + (size_t)(row0 + ai * 128 + m * 16) * 2048 + j0) = w;
;             }
	v_rcp_f32_e32 v156, v156
	v_cvt_pk_fp8_f32 v148, v64, v155
	v_med3_f32 v64, v152, s72, v236
	v_med3_f32 v152, v149, s72, v236
	v_mov_b32_e32 v149, v65
	v_cvt_pk_fp8_f32 v149, v64, v152
	v_mul_f32_e32 v154, v154, v156
	v_med3_f32 v64, v150, s72, v236
	v_med3_f32 v150, v151, s72, v236
	v_med3_f32 v153, v153, s72, v236
	v_med3_f32 v154, v154, s72, v236
	v_cvt_pk_fp8_f32 v149, v64, v150 op_sel:[0,0,1]
	v_or_b32_e32 v150, 32, v222
	v_cvt_pk_fp8_f32 v148, v153, v154 op_sel:[0,0,1]
	v_ashrrev_i32_e32 v151, 31, v150
	v_lshlrev_b64 v[150:151], 11, v[150:151]
	v_lshl_add_u64 v[150:151], s[16:17], 0, v[150:151]
	v_fmamk_f32 v64, v144, 0x3d000000, v208
	v_fmamk_f32 v140, v140, 0x3d000000, v200
	v_lshl_add_u64 v[150:151], v[150:151], 0, v[220:221]
	v_min_f32_e32 v64, 0x40e00000, v64
	v_min_f32_e32 v140, 0x40e00000, v140
	global_store_dwordx2 v[150:151], v[148:149], off
	v_mul_f32_e32 v144, 0x3fd9db23, v64
	v_mul_f32_e32 v148, 0x3fd9db23, v140
	v_mul_f32_e32 v144, 0xbfb8aa3b, v144
	v_mul_f32_e32 v148, 0xbfb8aa3b, v148
	v_exp_f32_e32 v144, v144
	v_exp_f32_e32 v148, v148
	v_fmamk_f32 v136, v136, 0x3d000000, v204
	v_med3_f32 v136, v136, s71, v235
	v_add_f32_e32 v136, 1.0, v136
	v_add_f32_e32 v144, 1.0, v144
	v_mul_f32_e32 v64, v64, v136
	v_add_f32_e32 v136, 1.0, v148
	v_rcp_f32_e32 v144, v144
	v_fmamk_f32 v132, v132, 0x3d000000, v196
	v_rcp_f32_e32 v136, v136
	v_med3_f32 v132, v132, s71, v235
	v_add_f32_e32 v132, 1.0, v132
	v_fmamk_f32 v141, v141, 0x3d000000, v201
	v_mul_f32_e32 v132, v140, v132
	v_min_f32_e32 v141, 0x40e00000, v141
	v_mul_f32_e32 v64, v64, v144
	v_mul_f32_e32 v136, v132, v136
	v_fmamk_f32 v132, v145, 0x3d000000, v209
	v_mul_f32_e32 v144, 0x3fd9db23, v141
	v_min_f32_e32 v132, 0x40e00000, v132
	v_mul_f32_e32 v144, 0xbfb8aa3b, v144
	v_mul_f32_e32 v140, 0x3fd9db23, v132
	v_exp_f32_e32 v144, v144
	v_mul_f32_e32 v140, 0xbfb8aa3b, v140
	v_fmamk_f32 v137, v137, 0x3d000000, v205
	v_exp_f32_e32 v140, v140
	v_med3_f32 v137, v137, s71, v235
	v_add_f32_e32 v137, 1.0, v137
	v_mul_f32_e32 v132, v132, v137
	v_fmamk_f32 v133, v133, 0x3d000000, v197
	v_add_f32_e32 v137, 1.0, v144
	v_rcp_f32_e32 v137, v137
	v_med3_f32 v133, v133, s71, v235
	v_add_f32_e32 v140, 1.0, v140
	v_add_f32_e32 v133, 1.0, v133
	v_rcp_f32_e32 v140, v140
	v_mul_f32_e32 v133, v141, v133
	v_fmamk_f32 v141, v142, 0x3d000000, v202
	v_min_f32_e32 v141, 0x40e00000, v141
	v_mul_f32_e32 v133, v133, v137
	v_fmamk_f32 v137, v146, 0x3d000000, v210
	v_mul_f32_e32 v142, 0x3fd9db23, v141
	v_min_f32_e32 v137, 0x40e00000, v137
	v_mul_f32_e32 v142, 0xbfb8aa3b, v142
	v_mul_f32_e32 v132, v132, v140
	v_mul_f32_e32 v140, 0x3fd9db23, v137
	v_exp_f32_e32 v142, v142
	v_mul_f32_e32 v140, 0xbfb8aa3b, v140
	v_fmamk_f32 v138, v138, 0x3d000000, v206
	v_fmamk_f32 v134, v134, 0x3d000000, v198
	v_exp_f32_e32 v140, v140
	v_med3_f32 v138, v138, s71, v235
	v_med3_f32 v134, v134, s71, v235
	v_add_f32_e32 v138, 1.0, v138
	v_add_f32_e32 v134, 1.0, v134
	v_mul_f32_e32 v137, v137, v138
	v_add_f32_e32 v138, 1.0, v142
	v_mul_f32_e32 v134, v141, v134
	v_fmamk_f32 v141, v143, 0x3d000000, v203
	v_rcp_f32_e32 v138, v138
	v_min_f32_e32 v141, 0x40e00000, v141
	v_add_f32_e32 v140, 1.0, v140
	v_mul_f32_e32 v142, 0x3fd9db23, v141
	v_rcp_f32_e32 v140, v140
	v_mul_f32_e32 v142, 0xbfb8aa3b, v142
	v_exp_f32_e32 v142, v142
	v_mul_f32_e32 v134, v134, v138
	v_fmamk_f32 v138, v147, 0x3d000000, v211
	v_fmamk_f32 v139, v139, 0x3d000000, v207
	v_min_f32_e32 v138, 0x40e00000, v138
	v_med3_f32 v139, v139, s71, v235
	v_mul_f32_e32 v137, v137, v140
	v_mul_f32_e32 v140, 0x3fd9db23, v138
	v_add_f32_e32 v139, 1.0, v139
	v_mul_f32_e32 v140, 0xbfb8aa3b, v140
	v_mul_f32_e32 v138, v138, v139
	v_add_f32_e32 v139, 1.0, v142
	v_exp_f32_e32 v140, v140
	v_fmamk_f32 v135, v135, 0x3d000000, v199
	v_rcp_f32_e32 v139, v139
	v_med3_f32 v135, v135, s71, v235
	v_add_f32_e32 v135, 1.0, v135
	v_mul_f32_e32 v135, v141, v135
	v_add_f32_e32 v140, 1.0, v140
	v_mul_f32_e32 v135, v135, v139
	v_med3_f32 v64, v64, s72, v236
	v_med3_f32 v139, v132, s72, v236
	v_mov_b32_e32 v132, v65
	v_rcp_f32_e32 v140, v140
	v_cvt_pk_fp8_f32 v132, v64, v139
	v_med3_f32 v64, v136, s72, v236
	v_med3_f32 v136, v133, s72, v236
	v_mov_b32_e32 v133, v65
	v_cvt_pk_fp8_f32 v133, v64, v136
	v_mul_f32_e32 v138, v138, v140
	v_med3_f32 v64, v134, s72, v236
	v_med3_f32 v134, v135, s72, v236
	v_med3_f32 v137, v137, s72, v236
	v_med3_f32 v138, v138, s72, v236
	v_cvt_pk_fp8_f32 v133, v64, v134 op_sel:[0,0,1]
	v_or_b32_e32 v134, 48, v222
	v_cvt_pk_fp8_f32 v132, v137, v138 op_sel:[0,0,1]
	v_ashrrev_i32_e32 v135, 31, v134
	v_lshlrev_b64 v[134:135], 11, v[134:135]
	v_lshl_add_u64 v[134:135], s[16:17], 0, v[134:135]
	v_lshl_add_u64 v[134:135], v[134:135], 0, v[220:221]
	global_store_dwordx2 v[134:135], v[132:133], off
	s_cbranch_vccnz .Lp9_fin4
; __device__ __forceinline__ float sigmoidf_(float x) { return __builtin_amdgcn_rcpf(1.f + __expf(-x)); }
;     __device__ __forceinline__ void operator()(const g8::Acc& acc, const g8::Unit& u, int wr, int wc, int fr, int fq) const {
;     ...
; #pragma unroll
;         for (int ai = 0; ai < 2; ++ai) {
;             if (u.hm <= ai * 128 + wr * 64) break;
; #pragma unroll
;             for (int m = 0; m < 4; ++m) {
;                 f32x4 ga = acc[ai][0][m][0] * WINV + g0, gb = acc[ai][0][m][1] * WINV + g1, ua = acc[ai][1][m][0] * WINV + u0, ub = acc[ai][1][m][1] * WINV + u1;
;                 f32x4 ha, hb;
; #pragma unroll
;                 for (int j = 0; j < 4; ++j) {
;                     const float gt = fminf(ga[j], 7.f), up = fminf(fmaxf(ua[j], -7.f), 7.f);
;                     ha[j] = (up + 1.f) * gt * sigmoidf_(1.702f * gt);
;                     const float gt2 = fminf(gb[j], 7.f), up2 = fminf(fmaxf(ub[j], -7.f), 7.f);
;                     hb[j] = (up2 + 1.f) * gt2 * sigmoidf_(1.702f * gt2);
;                 }
;                 u32x2 w; w.x = pk4_fp8s(ha[0], ha[1], ha[2], ha[3]); w.y = pk4_fp8s(hb[0], hb[1], hb[2], hb[3]);
;                 *(u32x2*)(HID + (size_t)(row0 + ai * 128 + m * 16) * 2048 + j0) = w;
;             }
	v_fmamk_f32 v64, v128, 0x3d000000, v208
	v_fmamk_f32 v124, v124, 0x3d000000, v200
	v_min_f32_e32 v64, 0x40e00000, v64
	v_min_f32_e32 v124, 0x40e00000, v124
	v_mul_f32_e32 v128, 0x3fd9db23, v64
	v_mul_f32_e32 v132, 0x3fd9db23, v124
	v_mul_f32_e32 v128, 0xbfb8aa3b, v128
	v_mul_f32_e32 v132, 0xbfb8aa3b, v132
	v_exp_f32_e32 v128, v128
	v_exp_f32_e32 v132, v132
	v_fmamk_f32 v120, v120, 0x3d000000, v204
	v_med3_f32 v120, v120, s71, v235
	v_add_f32_e32 v120, 1.0, v120
	v_add_f32_e32 v128, 1.0, v128
	v_mul_f32_e32 v64, v64, v120
	v_add_f32_e32 v120, 1.0, v132
	v_rcp_f32_e32 v128, v128
	v_fmamk_f32 v116, v116, 0x3d000000, v196
	v_rcp_f32_e32 v120, v120
	v_med3_f32 v116, v116, s71, v235
	v_add_f32_e32 v116, 1.0, v116
	v_fmamk_f32 v125, v125, 0x3d000000, v201
	v_mul_f32_e32 v116, v124, v116
	v_min_f32_e32 v125, 0x40e00000, v125
	v_mul_f32_e32 v64, v64, v128
	v_mul_f32_e32 v120, v116, v120
	v_fmamk_f32 v116, v129, 0x3d000000, v209
	v_mul_f32_e32 v128, 0x3fd9db23, v125
	v_min_f32_e32 v116, 0x40e00000, v116
	v_mul_f32_e32 v128, 0xbfb8aa3b, v128
	v_mul_f32_e32 v124, 0x3fd9db23, v116
	v_exp_f32_e32 v128, v128
	v_mul_f32_e32 v124, 0xbfb8aa3b, v124
	v_fmamk_f32 v121, v121, 0x3d000000, v205
	v_exp_f32_e32 v124, v124
	v_med3_f32 v121, v121, s71, v235
	v_add_f32_e32 v121, 1.0, v121
	v_mul_f32_e32 v116, v116, v121
	v_fmamk_f32 v117, v117, 0x3d000000, v197
	v_add_f32_e32 v121, 1.0, v128
	v_rcp_f32_e32 v121, v121
	v_med3_f32 v117, v117, s71, v235
	v_add_f32_e32 v124, 1.0, v124
	v_add_f32_e32 v117, 1.0, v117
	v_rcp_f32_e32 v124, v124
	v_mul_f32_e32 v117, v125, v117
	v_fmamk_f32 v125, v126, 0x3d000000, v202
	v_min_f32_e32 v125, 0x40e00000, v125
	v_mul_f32_e32 v117, v117, v121
	v_fmamk_f32 v121, v130, 0x3d000000, v210
	v_mul_f32_e32 v126, 0x3fd9db23, v125
	v_min_f32_e32 v121, 0x40e00000, v121
	v_mul_f32_e32 v126, 0xbfb8aa3b, v126
	v_mul_f32_e32 v116, v116, v124
	v_mul_f32_e32 v124, 0x3fd9db23, v121
	v_exp_f32_e32 v126, v126
	v_mul_f32_e32 v124, 0xbfb8aa3b, v124
	v_fmamk_f32 v122, v122, 0x3d000000, v206
	v_exp_f32_e32 v124, v124
	v_med3_f32 v122, v122, s71, v235
	v_fmamk_f32 v118, v118, 0x3d000000, v198
	v_add_f32_e32 v122, 1.0, v122
	v_med3_f32 v118, v118, s71, v235
	v_mul_f32_e32 v121, v121, v122
	v_add_f32_e32 v122, 1.0, v126
	v_add_f32_e32 v118, 1.0, v118
	v_rcp_f32_e32 v122, v122
	v_mul_f32_e32 v118, v125, v118
	v_fmamk_f32 v125, v127, 0x3d000000, v203
	v_add_f32_e32 v124, 1.0, v124
	v_min_f32_e32 v125, 0x40e00000, v125
	v_rcp_f32_e32 v124, v124
	v_mul_f32_e32 v126, 0x3fd9db23, v125
	v_mul_f32_e32 v126, 0xbfb8aa3b, v126
	v_mul_f32_e32 v118, v118, v122
	v_fmamk_f32 v122, v131, 0x3d000000, v211
	v_exp_f32_e32 v126, v126
	v_min_f32_e32 v122, 0x40e00000, v122
	v_fmamk_f32 v123, v123, 0x3d000000, v207
	v_mul_f32_e32 v121, v121, v124
	v_mul_f32_e32 v124, 0x3fd9db23, v122
	v_med3_f32 v123, v123, s71, v235
	v_mul_f32_e32 v124, 0xbfb8aa3b, v124
	v_add_f32_e32 v123, 1.0, v123
	v_exp_f32_e32 v124, v124
	v_mul_f32_e32 v122, v122, v123
	v_add_f32_e32 v123, 1.0, v126
	v_fmamk_f32 v119, v119, 0x3d000000, v199
	v_rcp_f32_e32 v123, v123
	v_med3_f32 v119, v119, s71, v235
	v_add_f32_e32 v119, 1.0, v119
	v_add_f32_e32 v124, 1.0, v124
	v_mul_f32_e32 v119, v125, v119
	v_rcp_f32_e32 v124, v124
	v_mul_f32_e32 v119, v119, v123
	v_med3_f32 v64, v64, s72, v236
	v_med3_f32 v123, v116, s72, v236
	v_mov_b32_e32 v116, v65
	v_cvt_pk_fp8_f32 v116, v64, v123
	v_med3_f32 v64, v120, s72, v236
	v_med3_f32 v120, v117, s72, v236
	v_mov_b32_e32 v117, v65
	v_cvt_pk_fp8_f32 v117, v64, v120
	v_mul_f32_e32 v122, v122, v124
	v_med3_f32 v121, v121, s72, v236
	v_med3_f32 v122, v122, s72, v236
	v_med3_f32 v64, v118, s72, v236
	v_med3_f32 v118, v119, s72, v236
	v_cvt_pk_fp8_f32 v116, v121, v122 op_sel:[0,0,1]
	v_cvt_pk_fp8_f32 v117, v64, v118 op_sel:[0,0,1]
	v_add_co_u32_e32 v118, vcc, s47, v66
	v_fmamk_f32 v64, v112, 0x3d000000, v208
	v_fmamk_f32 v108, v108, 0x3d000000, v200
	v_addc_co_u32_e32 v119, vcc, 0, v67, vcc
	v_min_f32_e32 v64, 0x40e00000, v64
	v_min_f32_e32 v108, 0x40e00000, v108
	global_store_dwordx2 v[118:119], v[116:117], off
	v_mul_f32_e32 v112, 0x3fd9db23, v64
	v_mul_f32_e32 v116, 0x3fd9db23, v108
	v_mul_f32_e32 v112, 0xbfb8aa3b, v112
	v_mul_f32_e32 v116, 0xbfb8aa3b, v116
	v_exp_f32_e32 v112, v112
	v_exp_f32_e32 v116, v116
	v_fmamk_f32 v104, v104, 0x3d000000, v204
	v_med3_f32 v104, v104, s71, v235
	v_add_f32_e32 v104, 1.0, v104
	v_add_f32_e32 v112, 1.0, v112
	v_mul_f32_e32 v64, v64, v104
	v_add_f32_e32 v104, 1.0, v116
	v_rcp_f32_e32 v112, v112
	v_fmamk_f32 v100, v100, 0x3d000000, v196
	v_rcp_f32_e32 v104, v104
	v_med3_f32 v100, v100, s71, v235
	v_add_f32_e32 v100, 1.0, v100
	v_fmamk_f32 v109, v109, 0x3d000000, v201
	v_mul_f32_e32 v100, v108, v100
	v_min_f32_e32 v109, 0x40e00000, v109
	v_mul_f32_e32 v64, v64, v112
	v_mul_f32_e32 v104, v100, v104
	v_fmamk_f32 v100, v113, 0x3d000000, v209
	v_mul_f32_e32 v112, 0x3fd9db23, v109
	v_min_f32_e32 v100, 0x40e00000, v100
	v_mul_f32_e32 v112, 0xbfb8aa3b, v112
	v_mul_f32_e32 v108, 0x3fd9db23, v100
	v_exp_f32_e32 v112, v112
	v_mul_f32_e32 v108, 0xbfb8aa3b, v108
	v_fmamk_f32 v105, v105, 0x3d000000, v205
	v_exp_f32_e32 v108, v108
	v_med3_f32 v105, v105, s71, v235
	v_add_f32_e32 v105, 1.0, v105
	v_mul_f32_e32 v100, v100, v105
	v_fmamk_f32 v101, v101, 0x3d000000, v197
	v_add_f32_e32 v105, 1.0, v112
	v_rcp_f32_e32 v105, v105
	v_med3_f32 v101, v101, s71, v235
	v_add_f32_e32 v108, 1.0, v108
	v_add_f32_e32 v101, 1.0, v101
	v_rcp_f32_e32 v108, v108
	v_mul_f32_e32 v101, v109, v101
	v_fmamk_f32 v109, v110, 0x3d000000, v202
	v_min_f32_e32 v109, 0x40e00000, v109
	v_mul_f32_e32 v101, v101, v105
	v_fmamk_f32 v105, v114, 0x3d000000, v210
	v_mul_f32_e32 v110, 0x3fd9db23, v109
; __device__ __forceinline__ float sigmoidf_(float x) { return __builtin_amdgcn_rcpf(1.f + __expf(-x)); }
;     __device__ __forceinline__ void operator()(const g8::Acc& acc, const g8::Unit& u, int wr, int wc, int fr, int fq) const {
;     ...
; #pragma unroll
;         for (int ai = 0; ai < 2; ++ai) {
;             if (u.hm <= ai * 128 + wr * 64) break;
; #pragma unroll
;             for (int m = 0; m < 4; ++m) {
;                 f32x4 ga = acc[ai][0][m][0] * WINV + g0, gb = acc[ai][0][m][1] * WINV + g1, ua = acc[ai][1][m][0] * WINV + u0, ub = acc[ai][1][m][1] * WINV + u1;
;                 f32x4 ha, hb;
; #pragma unroll
;                 for (int j = 0; j < 4; ++j) {
;                     const float gt = fminf(ga[j], 7.f), up = fminf(fmaxf(ua[j], -7.f), 7.f);
;                     ha[j] = (up + 1.f) * gt * sigmoidf_(1.702f * gt);
;                     const float gt2 = fminf(gb[j], 7.f), up2 = fminf(fmaxf(ub[j], -7.f), 7.f);
;                     hb[j] = (up2 + 1.f) * gt2 * sigmoidf_(1.702f * gt2);
;                 }
;                 u32x2 w; w.x = pk4_fp8s(ha[0], ha[1], ha[2], ha[3]); w.y = pk4_fp8s(hb[0], hb[1], hb[2], hb[3]);
;                 *(u32x2*)(HID + (size_t)(row0 + ai * 128 + m * 16) * 2048 + j0) = w;
;             }
	v_min_f32_e32 v105, 0x40e00000, v105
	v_mul_f32_e32 v110, 0xbfb8aa3b, v110
	v_mul_f32_e32 v100, v100, v108
	v_mul_f32_e32 v108, 0x3fd9db23, v105
	v_exp_f32_e32 v110, v110
	v_mul_f32_e32 v108, 0xbfb8aa3b, v108
	v_fmamk_f32 v106, v106, 0x3d000000, v206
	v_exp_f32_e32 v108, v108
	v_med3_f32 v106, v106, s71, v235
	v_fmamk_f32 v102, v102, 0x3d000000, v198
	v_add_f32_e32 v106, 1.0, v106
	v_med3_f32 v102, v102, s71, v235
	v_mul_f32_e32 v105, v105, v106
	v_add_f32_e32 v106, 1.0, v110
	v_add_f32_e32 v102, 1.0, v102
	v_rcp_f32_e32 v106, v106
	v_mul_f32_e32 v102, v109, v102
	v_fmamk_f32 v109, v111, 0x3d000000, v203
	v_add_f32_e32 v108, 1.0, v108
	v_min_f32_e32 v109, 0x40e00000, v109
	v_rcp_f32_e32 v108, v108
	v_mul_f32_e32 v110, 0x3fd9db23, v109
	v_mul_f32_e32 v110, 0xbfb8aa3b, v110
	v_mul_f32_e32 v102, v102, v106
	v_fmamk_f32 v106, v115, 0x3d000000, v211
	v_exp_f32_e32 v110, v110
	v_min_f32_e32 v106, 0x40e00000, v106
	v_fmamk_f32 v107, v107, 0x3d000000, v207
	v_mul_f32_e32 v105, v105, v108
	v_mul_f32_e32 v108, 0x3fd9db23, v106
	v_med3_f32 v107, v107, s71, v235
	v_mul_f32_e32 v108, 0xbfb8aa3b, v108
	v_add_f32_e32 v107, 1.0, v107
	v_exp_f32_e32 v108, v108
	v_mul_f32_e32 v106, v106, v107
	v_add_f32_e32 v107, 1.0, v110
	v_fmamk_f32 v103, v103, 0x3d000000, v199
	v_rcp_f32_e32 v107, v107
	v_med3_f32 v103, v103, s71, v235
	v_add_f32_e32 v103, 1.0, v103
	v_add_f32_e32 v108, 1.0, v108
	v_mul_f32_e32 v103, v109, v103
	v_rcp_f32_e32 v108, v108
	v_mul_f32_e32 v103, v103, v107
	v_med3_f32 v64, v64, s72, v236
	v_med3_f32 v107, v100, s72, v236
	v_mov_b32_e32 v100, v65
	v_cvt_pk_fp8_f32 v100, v64, v107
	v_med3_f32 v64, v104, s72, v236
	v_med3_f32 v104, v101, s72, v236
	v_mov_b32_e32 v101, v65
	v_cvt_pk_fp8_f32 v101, v64, v104
	v_mul_f32_e32 v106, v106, v108
	v_med3_f32 v105, v105, s72, v236
	v_med3_f32 v106, v106, s72, v236
	v_med3_f32 v64, v102, s72, v236
	v_med3_f32 v102, v103, s72, v236
	v_cvt_pk_fp8_f32 v100, v105, v106 op_sel:[0,0,1]
	v_cvt_pk_fp8_f32 v101, v64, v102 op_sel:[0,0,1]
	v_add_co_u32_e32 v102, vcc, s48, v66
	v_fmamk_f32 v64, v96, 0x3d000000, v208
	v_fmamk_f32 v92, v92, 0x3d000000, v200
	v_addc_co_u32_e32 v103, vcc, 0, v67, vcc
	v_min_f32_e32 v64, 0x40e00000, v64
	v_min_f32_e32 v92, 0x40e00000, v92
	global_store_dwordx2 v[102:103], v[100:101], off
	v_mul_f32_e32 v96, 0x3fd9db23, v64
	v_mul_f32_e32 v100, 0x3fd9db23, v92
	v_mul_f32_e32 v96, 0xbfb8aa3b, v96
	v_mul_f32_e32 v100, 0xbfb8aa3b, v100
	v_exp_f32_e32 v96, v96
	v_exp_f32_e32 v100, v100
	v_fmamk_f32 v88, v88, 0x3d000000, v204
	v_med3_f32 v88, v88, s71, v235
	v_add_f32_e32 v88, 1.0, v88
	v_add_f32_e32 v96, 1.0, v96
	v_mul_f32_e32 v64, v64, v88
	v_add_f32_e32 v88, 1.0, v100
	v_rcp_f32_e32 v96, v96
	v_fmamk_f32 v84, v84, 0x3d000000, v196
	v_rcp_f32_e32 v88, v88
	v_med3_f32 v84, v84, s71, v235
	v_add_f32_e32 v84, 1.0, v84
	v_fmamk_f32 v93, v93, 0x3d000000, v201
	v_mul_f32_e32 v84, v92, v84
	v_min_f32_e32 v93, 0x40e00000, v93
	v_mul_f32_e32 v64, v64, v96
	v_mul_f32_e32 v88, v84, v88
	v_fmamk_f32 v84, v97, 0x3d000000, v209
	v_mul_f32_e32 v96, 0x3fd9db23, v93
	v_min_f32_e32 v84, 0x40e00000, v84
	v_mul_f32_e32 v96, 0xbfb8aa3b, v96
	v_mul_f32_e32 v92, 0x3fd9db23, v84
	v_exp_f32_e32 v96, v96
	v_mul_f32_e32 v92, 0xbfb8aa3b, v92
	v_fmamk_f32 v89, v89, 0x3d000000, v205
	v_exp_f32_e32 v92, v92
	v_med3_f32 v89, v89, s71, v235
	v_add_f32_e32 v89, 1.0, v89
	v_mul_f32_e32 v84, v84, v89
	v_fmamk_f32 v85, v85, 0x3d000000, v197
	v_add_f32_e32 v89, 1.0, v96
	v_rcp_f32_e32 v89, v89
	v_med3_f32 v85, v85, s71, v235
	v_add_f32_e32 v92, 1.0, v92
	v_add_f32_e32 v85, 1.0, v85
	v_rcp_f32_e32 v92, v92
	v_mul_f32_e32 v85, v93, v85
	v_fmamk_f32 v93, v94, 0x3d000000, v202
	v_min_f32_e32 v93, 0x40e00000, v93
	v_mul_f32_e32 v85, v85, v89
	v_fmamk_f32 v89, v98, 0x3d000000, v210
	v_mul_f32_e32 v94, 0x3fd9db23, v93
	v_min_f32_e32 v89, 0x40e00000, v89
	v_mul_f32_e32 v94, 0xbfb8aa3b, v94
	v_mul_f32_e32 v84, v84, v92
	v_mul_f32_e32 v92, 0x3fd9db23, v89
	v_exp_f32_e32 v94, v94
	v_mul_f32_e32 v92, 0xbfb8aa3b, v92
	v_fmamk_f32 v90, v90, 0x3d000000, v206
	v_exp_f32_e32 v92, v92
	v_med3_f32 v90, v90, s71, v235
	v_fmamk_f32 v86, v86, 0x3d000000, v198
	v_add_f32_e32 v90, 1.0, v90
	v_med3_f32 v86, v86, s71, v235
	v_mul_f32_e32 v89, v89, v90
	v_add_f32_e32 v90, 1.0, v94
	v_add_f32_e32 v86, 1.0, v86
	v_rcp_f32_e32 v90, v90
	v_mul_f32_e32 v86, v93, v86
	v_fmamk_f32 v93, v95, 0x3d000000, v203
	v_add_f32_e32 v92, 1.0, v92
	v_min_f32_e32 v93, 0x40e00000, v93
	v_rcp_f32_e32 v92, v92
	v_mul_f32_e32 v94, 0x3fd9db23, v93
	v_mul_f32_e32 v94, 0xbfb8aa3b, v94
	v_mul_f32_e32 v86, v86, v90
	v_fmamk_f32 v90, v99, 0x3d000000, v211
	v_exp_f32_e32 v94, v94
	v_min_f32_e32 v90, 0x40e00000, v90
	v_fmamk_f32 v91, v91, 0x3d000000, v207
	v_mul_f32_e32 v89, v89, v92
	v_mul_f32_e32 v92, 0x3fd9db23, v90
	v_med3_f32 v91, v91, s71, v235
	v_mul_f32_e32 v92, 0xbfb8aa3b, v92
	v_add_f32_e32 v91, 1.0, v91
	v_exp_f32_e32 v92, v92
	v_mul_f32_e32 v90, v90, v91
	v_add_f32_e32 v91, 1.0, v94
	v_fmamk_f32 v87, v87, 0x3d000000, v199
	v_rcp_f32_e32 v91, v91
	v_med3_f32 v87, v87, s71, v235
	v_add_f32_e32 v87, 1.0, v87
	v_add_f32_e32 v92, 1.0, v92
	v_mul_f32_e32 v87, v93, v87
	v_rcp_f32_e32 v92, v92
	v_mul_f32_e32 v87, v87, v91
	v_med3_f32 v64, v64, s72, v236
	v_med3_f32 v91, v84, s72, v236
	v_mov_b32_e32 v84, v65
	v_cvt_pk_fp8_f32 v84, v64, v91
	v_med3_f32 v64, v88, s72, v236
	v_med3_f32 v88, v85, s72, v236
	v_mov_b32_e32 v85, v65
	v_cvt_pk_fp8_f32 v85, v64, v88
	v_mul_f32_e32 v90, v90, v92
	v_med3_f32 v89, v89, s72, v236
	v_med3_f32 v90, v90, s72, v236
	v_med3_f32 v64, v86, s72, v236
	v_med3_f32 v86, v87, s72, v236
	v_cvt_pk_fp8_f32 v84, v89, v90 op_sel:[0,0,1]
; __device__ __forceinline__ float sigmoidf_(float x) { return __builtin_amdgcn_rcpf(1.f + __expf(-x)); }
;     __device__ __forceinline__ void operator()(const g8::Acc& acc, const g8::Unit& u, int wr, int wc, int fr, int fq) const {
;     ...
; #pragma unroll
;         for (int ai = 0; ai < 2; ++ai) {
;             if (u.hm <= ai * 128 + wr * 64) break;
; #pragma unroll
;             for (int m = 0; m < 4; ++m) {
;                 f32x4 ga = acc[ai][0][m][0] * WINV + g0, gb = acc[ai][0][m][1] * WINV + g1, ua = acc[ai][1][m][0] * WINV + u0, ub = acc[ai][1][m][1] * WINV + u1;
;                 f32x4 ha, hb;
; #pragma unroll
;                 for (int j = 0; j < 4; ++j) {
;                     const float gt = fminf(ga[j], 7.f), up = fminf(fmaxf(ua[j], -7.f), 7.f);
;                     ha[j] = (up + 1.f) * gt * sigmoidf_(1.702f * gt);
;                     const float gt2 = fminf(gb[j], 7.f), up2 = fminf(fmaxf(ub[j], -7.f), 7.f);
;                     hb[j] = (up2 + 1.f) * gt2 * sigmoidf_(1.702f * gt2);
;                 }
;                 u32x2 w; w.x = pk4_fp8s(ha[0], ha[1], ha[2], ha[3]); w.y = pk4_fp8s(hb[0], hb[1], hb[2], hb[3]);
;                 *(u32x2*)(HID + (size_t)(row0 + ai * 128 + m * 16) * 2048 + j0) = w;
;             }
;         }
	v_cvt_pk_fp8_f32 v85, v64, v86 op_sel:[0,0,1]
	v_add_co_u32_e32 v86, vcc, s49, v66
	v_fmamk_f32 v64, v80, 0x3d000000, v208
	v_fmamk_f32 v76, v76, 0x3d000000, v200
	v_addc_co_u32_e32 v87, vcc, 0, v67, vcc
	v_min_f32_e32 v64, 0x40e00000, v64
	v_min_f32_e32 v76, 0x40e00000, v76
	global_store_dwordx2 v[86:87], v[84:85], off
	v_mul_f32_e32 v80, 0x3fd9db23, v64
	v_mul_f32_e32 v84, 0x3fd9db23, v76
	v_mul_f32_e32 v80, 0xbfb8aa3b, v80
	v_mul_f32_e32 v84, 0xbfb8aa3b, v84
	v_exp_f32_e32 v80, v80
	v_exp_f32_e32 v84, v84
	v_fmamk_f32 v72, v72, 0x3d000000, v204
	v_med3_f32 v72, v72, s71, v235
	v_add_f32_e32 v72, 1.0, v72
	v_add_f32_e32 v80, 1.0, v80
	v_mul_f32_e32 v64, v64, v72
	v_add_f32_e32 v72, 1.0, v84
	v_rcp_f32_e32 v80, v80
	v_fmamk_f32 v68, v68, 0x3d000000, v196
	v_rcp_f32_e32 v72, v72
	v_med3_f32 v68, v68, s71, v235
	v_add_f32_e32 v68, 1.0, v68
	v_fmamk_f32 v77, v77, 0x3d000000, v201
	v_mul_f32_e32 v68, v76, v68
	v_min_f32_e32 v77, 0x40e00000, v77
	v_mul_f32_e32 v64, v64, v80
	v_mul_f32_e32 v72, v68, v72
	v_fmamk_f32 v68, v81, 0x3d000000, v209
	v_mul_f32_e32 v80, 0x3fd9db23, v77
	v_min_f32_e32 v68, 0x40e00000, v68
	v_mul_f32_e32 v80, 0xbfb8aa3b, v80
	v_mul_f32_e32 v76, 0x3fd9db23, v68
	v_exp_f32_e32 v80, v80
	v_mul_f32_e32 v76, 0xbfb8aa3b, v76
	v_fmamk_f32 v73, v73, 0x3d000000, v205
	v_exp_f32_e32 v76, v76
	v_med3_f32 v73, v73, s71, v235
	v_add_f32_e32 v73, 1.0, v73
	v_mul_f32_e32 v68, v68, v73
	v_add_f32_e32 v73, 1.0, v80
	v_fmamk_f32 v69, v69, 0x3d000000, v197
	v_rcp_f32_e32 v73, v73
	v_add_f32_e32 v76, 1.0, v76
	v_med3_f32 v69, v69, s71, v235
	v_rcp_f32_e32 v76, v76
	v_add_f32_e32 v69, 1.0, v69
	v_mul_f32_e32 v69, v77, v69
	v_fmamk_f32 v77, v78, 0x3d000000, v202
	v_mul_f32_e32 v69, v69, v73
	v_fmamk_f32 v73, v82, 0x3d000000, v210
	v_min_f32_e32 v77, 0x40e00000, v77
	v_min_f32_e32 v73, 0x40e00000, v73
	v_mul_f32_e32 v78, 0x3fd9db23, v77
	v_mul_f32_e32 v68, v68, v76
	v_mul_f32_e32 v76, 0x3fd9db23, v73
	v_mul_f32_e32 v78, 0xbfb8aa3b, v78
	v_mul_f32_e32 v76, 0xbfb8aa3b, v76
	v_exp_f32_e32 v78, v78
	v_exp_f32_e32 v76, v76
	v_fmamk_f32 v74, v74, 0x3d000000, v206
	v_med3_f32 v74, v74, s71, v235
	v_fmamk_f32 v70, v70, 0x3d000000, v198
	v_add_f32_e32 v74, 1.0, v74
	v_med3_f32 v70, v70, s71, v235
	v_mul_f32_e32 v73, v73, v74
	v_add_f32_e32 v74, 1.0, v78
	v_add_f32_e32 v70, 1.0, v70
	v_fmac_f32_e32 v203, 0x3d000000, v79
	v_add_f32_e32 v76, 1.0, v76
	v_rcp_f32_e32 v74, v74
	v_mul_f32_e32 v70, v77, v70
	v_min_f32_e32 v77, 0x40e00000, v203
	v_rcp_f32_e32 v76, v76
	v_mul_f32_e32 v78, 0x3fd9db23, v77
	v_mul_f32_e32 v78, 0xbfb8aa3b, v78
	v_fmac_f32_e32 v211, 0x3d000000, v83
	v_exp_f32_e32 v78, v78
	v_mul_f32_e32 v70, v70, v74
	v_min_f32_e32 v74, 0x40e00000, v211
	v_mul_f32_e32 v73, v73, v76
	v_mul_f32_e32 v76, 0x3fd9db23, v74
	v_mul_f32_e32 v76, 0xbfb8aa3b, v76
	v_fmac_f32_e32 v207, 0x3d000000, v75
	v_exp_f32_e32 v76, v76
	v_med3_f32 v75, v207, s71, v235
	v_fmac_f32_e32 v199, 0x3d000000, v71
	v_add_f32_e32 v71, 1.0, v78
	v_add_f32_e32 v75, 1.0, v75
	v_rcp_f32_e32 v71, v71
	v_mul_f32_e32 v74, v74, v75
	v_med3_f32 v75, v199, s71, v235
	v_add_f32_e32 v75, 1.0, v75
	v_add_f32_e32 v76, 1.0, v76
	v_mul_f32_e32 v75, v77, v75
	v_rcp_f32_e32 v76, v76
	v_mul_f32_e32 v71, v75, v71
	v_med3_f32 v64, v64, s72, v236
	v_med3_f32 v75, v68, s72, v236
	v_mov_b32_e32 v68, v65
	v_cvt_pk_fp8_f32 v68, v64, v75
	v_med3_f32 v64, v72, s72, v236
	v_med3_f32 v72, v69, s72, v236
	v_mov_b32_e32 v69, v65
	v_cvt_pk_fp8_f32 v69, v64, v72
	v_mul_f32_e32 v74, v74, v76
	v_med3_f32 v73, v73, s72, v236
	v_med3_f32 v74, v74, s72, v236
	v_med3_f32 v64, v70, s72, v236
	v_med3_f32 v70, v71, s72, v236
	v_cvt_pk_fp8_f32 v68, v73, v74 op_sel:[0,0,1]
	v_cvt_pk_fp8_f32 v69, v64, v70 op_sel:[0,0,1]
	v_add_co_u32_e32 v66, vcc, 0x58000, v66
	s_nop 1
	v_addc_co_u32_e32 v67, vcc, 0, v67, vcc
	global_store_dwordx2 v[66:67], v[68:69], off
	s_cmp_eq_u32 s99, 0
	s_cbranch_scc1 .Lp9f8_nofin
	s_sub_i32 s100, s99, 0x10000
	s_lshr_b32 s100, s100, 10
	s_lshl_b32 s100, s100, 22
	s_and_b32 s101, s99, 63
	s_lshl_b32 s101, s101, 16
	s_add_i32 s100, s100, s101
	s_bfe_u32 s101, s99, 0x40006
	s_lshl_b32 s101, s101, 7
	s_add_i32 s100, s100, s101
	v_mbcnt_lo_u32_b32 v244, -1, 0
	v_mbcnt_hi_u32_b32 v244, -1, v244
	v_lshrrev_b32_e32 v245, 3, v244
	v_and_b32_e32 v246, 7, v244
	v_lshlrev_b32_e32 v245, 4, v245
	v_lshl_or_b32 v245, v246, 13, v245
	v_add_u32_e32 v245, s100, v245
	v_readlane_b32 s100, v254, 48
	v_readlane_b32 s101, v254, 49
	s_add_u32 s100, s100, 0x14d59400
	s_addc_u32 s101, s101, 0
	s_waitcnt vmcnt(8)
	v_mul_f32_e32 v246, 0x42000000, v0
	v_mul_f32_e32 v247, 0x42000000, v4
	v_mov_b32_e32 v248, 0
	v_cvt_pk_fp8_f32 v248, v246, v247
	v_mul_f32_e32 v246, 0x42000000, v8
	v_mul_f32_e32 v247, 0x42000000, v12
	v_cvt_pk_fp8_f32 v248, v246, v247 op_sel:[0,0,1]
	v_mul_f32_e32 v246, 0x42000000, v16
	v_mul_f32_e32 v247, 0x42000000, v20
	v_mov_b32_e32 v249, 0
	v_cvt_pk_fp8_f32 v249, v246, v247
	v_mul_f32_e32 v246, 0x42000000, v24
	v_mul_f32_e32 v247, 0x42000000, v28
	v_cvt_pk_fp8_f32 v249, v246, v247 op_sel:[0,0,1]
	v_mul_f32_e32 v246, 0x42000000, v32
	v_mul_f32_e32 v247, 0x42000000, v36
	v_mov_b32_e32 v250, 0
	v_cvt_pk_fp8_f32 v250, v246, v247
	v_mul_f32_e32 v246, 0x42000000, v40
	v_mul_f32_e32 v247, 0x42000000, v44
	v_cvt_pk_fp8_f32 v250, v246, v247 op_sel:[0,0,1]
	v_mul_f32_e32 v246, 0x42000000, v48
	v_mul_f32_e32 v247, 0x42000000, v52
	v_mov_b32_e32 v251, 0
	v_cvt_pk_fp8_f32 v251, v246, v247
	v_mul_f32_e32 v246, 0x42000000, v56
	v_mul_f32_e32 v247, 0x42000000, v60
	v_cvt_pk_fp8_f32 v251, v246, v247 op_sel:[0,0,1]
	s_nop 0
	global_store_dwordx4 v245, v[248:251], s[100:101]
	v_mul_f32_e32 v246, 0x42000000, v1
	v_mul_f32_e32 v247, 0x42000000, v5
	v_mov_b32_e32 v248, 0
	v_cvt_pk_fp8_f32 v248, v246, v247
	v_mul_f32_e32 v246, 0x42000000, v9
	v_mul_f32_e32 v247, 0x42000000, v13
	v_cvt_pk_fp8_f32 v248, v246, v247 op_sel:[0,0,1]
	v_mul_f32_e32 v246, 0x42000000, v17
	v_mul_f32_e32 v247, 0x42000000, v21
	v_mov_b32_e32 v249, 0
	v_cvt_pk_fp8_f32 v249, v246, v247
	v_mul_f32_e32 v246, 0x42000000, v25
	v_mul_f32_e32 v247, 0x42000000, v29
	v_cvt_pk_fp8_f32 v249, v246, v247 op_sel:[0,0,1]
	v_mul_f32_e32 v246, 0x42000000, v33
	v_mul_f32_e32 v247, 0x42000000, v37
	v_mov_b32_e32 v250, 0
	v_cvt_pk_fp8_f32 v250, v246, v247
	v_mul_f32_e32 v246, 0x42000000, v41
	v_mul_f32_e32 v247, 0x42000000, v45
	v_cvt_pk_fp8_f32 v250, v246, v247 op_sel:[0,0,1]
	v_mul_f32_e32 v246, 0x42000000, v49
	v_mul_f32_e32 v247, 0x42000000, v53
	v_mov_b32_e32 v251, 0
	v_cvt_pk_fp8_f32 v251, v246, v247
	v_mul_f32_e32 v246, 0x42000000, v57
	v_mul_f32_e32 v247, 0x42000000, v61
	v_cvt_pk_fp8_f32 v251, v246, v247 op_sel:[0,0,1]
	s_nop 0
	global_store_dwordx4 v245, v[248:251], s[100:101] offset:2048
	v_add_u32_e32 v245, 0x1000, v245
	v_mul_f32_e32 v246, 0x42000000, v2
	v_mul_f32_e32 v247, 0x42000000, v6
	v_mov_b32_e32 v248, 0
	v_cvt_pk_fp8_f32 v248, v246, v247
	v_mul_f32_e32 v246, 0x42000000, v10
	v_mul_f32_e32 v247, 0x42000000, v14
	v_cvt_pk_fp8_f32 v248, v246, v247 op_sel:[0,0,1]
	v_mul_f32_e32 v246, 0x42000000, v18
	v_mul_f32_e32 v247, 0x42000000, v22
	v_mov_b32_e32 v249, 0
	v_cvt_pk_fp8_f32 v249, v246, v247
	v_mul_f32_e32 v246, 0x42000000, v26
	v_mul_f32_e32 v247, 0x42000000, v30
	v_cvt_pk_fp8_f32 v249, v246, v247 op_sel:[0,0,1]
	v_mul_f32_e32 v246, 0x42000000, v34
	v_mul_f32_e32 v247, 0x42000000, v38
	v_mov_b32_e32 v250, 0
	v_cvt_pk_fp8_f32 v250, v246, v247
	v_mul_f32_e32 v246, 0x42000000, v42
	v_mul_f32_e32 v247, 0x42000000, v46
	v_cvt_pk_fp8_f32 v250, v246, v247 op_sel:[0,0,1]
	v_mul_f32_e32 v246, 0x42000000, v50
	v_mul_f32_e32 v247, 0x42000000, v54
	v_mov_b32_e32 v251, 0
	v_cvt_pk_fp8_f32 v251, v246, v247
	v_mul_f32_e32 v246, 0x42000000, v58
	v_mul_f32_e32 v247, 0x42000000, v62
	v_cvt_pk_fp8_f32 v251, v246, v247 op_sel:[0,0,1]
	s_nop 0
	global_store_dwordx4 v245, v[248:251], s[100:101]
	v_mul_f32_e32 v246, 0x42000000, v3
	v_mul_f32_e32 v247, 0x42000000, v7
	v_mov_b32_e32 v248, 0
	v_cvt_pk_fp8_f32 v248, v246, v247
	v_mul_f32_e32 v246, 0x42000000, v11
	v_mul_f32_e32 v247, 0x42000000, v15
	v_cvt_pk_fp8_f32 v248, v246, v247 op_sel:[0,0,1]
	v_mul_f32_e32 v246, 0x42000000, v19
	v_mul_f32_e32 v247, 0x42000000, v23
	v_mov_b32_e32 v249, 0
	v_cvt_pk_fp8_f32 v249, v246, v247
	v_mul_f32_e32 v246, 0x42000000, v27
	v_mul_f32_e32 v247, 0x42000000, v31
	v_cvt_pk_fp8_f32 v249, v246, v247 op_sel:[0,0,1]
	v_mul_f32_e32 v246, 0x42000000, v35
	v_mul_f32_e32 v247, 0x42000000, v39
	v_mov_b32_e32 v250, 0
	v_cvt_pk_fp8_f32 v250, v246, v247
	v_mul_f32_e32 v246, 0x42000000, v43
	v_mul_f32_e32 v247, 0x42000000, v47
	v_cvt_pk_fp8_f32 v250, v246, v247 op_sel:[0,0,1]
	v_mul_f32_e32 v246, 0x42000000, v51
	v_mul_f32_e32 v247, 0x42000000, v55
	v_mov_b32_e32 v251, 0
	v_cvt_pk_fp8_f32 v251, v246, v247
	v_mul_f32_e32 v246, 0x42000000, v59
	v_mul_f32_e32 v247, 0x42000000, v63
	v_cvt_pk_fp8_f32 v251, v246, v247 op_sel:[0,0,1]
	s_nop 0
	global_store_dwordx4 v245, v[248:251], s[100:101] offset:2048
	s_add_i32 s98, s98, 0x800
	s_mov_b32 s99, 0
.Lp9f8_nofin:
	s_branch .LBB0_1139
.Lp9_fin4:
	s_cmp_eq_u32 s99, 0
	s_cbranch_scc1 .Lp9f4_nofin
	s_sub_i32 s100, s99, 0x10000
	s_lshr_b32 s100, s100, 10
	s_lshl_b32 s100, s100, 22
	s_and_b32 s101, s99, 63
	s_lshl_b32 s101, s101, 16
	s_add_i32 s100, s100, s101
	s_bfe_u32 s101, s99, 0x40006
	s_lshl_b32 s101, s101, 7
	s_add_i32 s100, s100, s101
	v_mbcnt_lo_u32_b32 v244, -1, 0
	v_mbcnt_hi_u32_b32 v244, -1, v244
	v_lshrrev_b32_e32 v245, 3, v244
	v_and_b32_e32 v246, 7, v244
	v_lshlrev_b32_e32 v245, 4, v245
	v_lshl_or_b32 v245, v246, 13, v245
	v_add_u32_e32 v245, s100, v245
	v_readlane_b32 s100, v254, 48
	v_readlane_b32 s101, v254, 49
	s_add_u32 s100, s100, 0x14d59400
	s_addc_u32 s101, s101, 0
	s_waitcnt vmcnt(4)
	v_mul_f32_e32 v246, 0x42000000, v0
	v_mul_f32_e32 v247, 0x42000000, v4
	v_mov_b32_e32 v248, 0
	v_cvt_pk_fp8_f32 v248, v246, v247
	v_mul_f32_e32 v246, 0x42000000, v8
	v_mul_f32_e32 v247, 0x42000000, v12
	v_cvt_pk_fp8_f32 v248, v246, v247 op_sel:[0,0,1]
	v_mul_f32_e32 v246, 0x42000000, v16
	v_mul_f32_e32 v247, 0x42000000, v20
	v_mov_b32_e32 v249, 0
	v_cvt_pk_fp8_f32 v249, v246, v247
	v_mul_f32_e32 v246, 0x42000000, v24
	v_mul_f32_e32 v247, 0x42000000, v28
	v_cvt_pk_fp8_f32 v249, v246, v247 op_sel:[0,0,1]
	v_mul_f32_e32 v246, 0x42000000, v32
	v_mul_f32_e32 v247, 0x42000000, v36
	v_mov_b32_e32 v250, 0
	v_cvt_pk_fp8_f32 v250, v246, v247
	v_mul_f32_e32 v246, 0x42000000, v40
	v_mul_f32_e32 v247, 0x42000000, v44
	v_cvt_pk_fp8_f32 v250, v246, v247 op_sel:[0,0,1]
	v_mul_f32_e32 v246, 0x42000000, v48
	v_mul_f32_e32 v247, 0x42000000, v52
	v_mov_b32_e32 v251, 0
	v_cvt_pk_fp8_f32 v251, v246, v247
	v_mul_f32_e32 v246, 0x42000000, v56
	v_mul_f32_e32 v247, 0x42000000, v60
	v_cvt_pk_fp8_f32 v251, v246, v247 op_sel:[0,0,1]
	s_nop 0
	global_store_dwordx4 v245, v[248:251], s[100:101]
	v_mul_f32_e32 v246, 0x42000000, v1
	v_mul_f32_e32 v247, 0x42000000, v5
	v_mov_b32_e32 v248, 0
	v_cvt_pk_fp8_f32 v248, v246, v247
	v_mul_f32_e32 v246, 0x42000000, v9
	v_mul_f32_e32 v247, 0x42000000, v13
	v_cvt_pk_fp8_f32 v248, v246, v247 op_sel:[0,0,1]
	v_mul_f32_e32 v246, 0x42000000, v17
	v_mul_f32_e32 v247, 0x42000000, v21
	v_mov_b32_e32 v249, 0
	v_cvt_pk_fp8_f32 v249, v246, v247
	v_mul_f32_e32 v246, 0x42000000, v25
	v_mul_f32_e32 v247, 0x42000000, v29
	v_cvt_pk_fp8_f32 v249, v246, v247 op_sel:[0,0,1]
	v_mul_f32_e32 v246, 0x42000000, v33
	v_mul_f32_e32 v247, 0x42000000, v37
	v_mov_b32_e32 v250, 0
	v_cvt_pk_fp8_f32 v250, v246, v247
	v_mul_f32_e32 v246, 0x42000000, v41
	v_mul_f32_e32 v247, 0x42000000, v45
	v_cvt_pk_fp8_f32 v250, v246, v247 op_sel:[0,0,1]
	v_mul_f32_e32 v246, 0x42000000, v49
	v_mul_f32_e32 v247, 0x42000000, v53
	v_mov_b32_e32 v251, 0
	v_cvt_pk_fp8_f32 v251, v246, v247
	v_mul_f32_e32 v246, 0x42000000, v57
	v_mul_f32_e32 v247, 0x42000000, v61
	v_cvt_pk_fp8_f32 v251, v246, v247 op_sel:[0,0,1]
	s_nop 0
	global_store_dwordx4 v245, v[248:251], s[100:101] offset:2048
	v_add_u32_e32 v245, 0x1000, v245
	v_mul_f32_e32 v246, 0x42000000, v2
	v_mul_f32_e32 v247, 0x42000000, v6
	v_mov_b32_e32 v248, 0
	v_cvt_pk_fp8_f32 v248, v246, v247
	v_mul_f32_e32 v246, 0x42000000, v10
	v_mul_f32_e32 v247, 0x42000000, v14
	v_cvt_pk_fp8_f32 v248, v246, v247 op_sel:[0,0,1]
	v_mul_f32_e32 v246, 0x42000000, v18
	v_mul_f32_e32 v247, 0x42000000, v22
	v_mov_b32_e32 v249, 0
	v_cvt_pk_fp8_f32 v249, v246, v247
	v_mul_f32_e32 v246, 0x42000000, v26
	v_mul_f32_e32 v247, 0x42000000, v30
	v_cvt_pk_fp8_f32 v249, v246, v247 op_sel:[0,0,1]
	v_mul_f32_e32 v246, 0x42000000, v34
	v_mul_f32_e32 v247, 0x42000000, v38
	v_mov_b32_e32 v250, 0
	v_cvt_pk_fp8_f32 v250, v246, v247
	v_mul_f32_e32 v246, 0x42000000, v42
	v_mul_f32_e32 v247, 0x42000000, v46
	v_cvt_pk_fp8_f32 v250, v246, v247 op_sel:[0,0,1]
	v_mul_f32_e32 v246, 0x42000000, v50
	v_mul_f32_e32 v247, 0x42000000, v54
	v_mov_b32_e32 v251, 0
	v_cvt_pk_fp8_f32 v251, v246, v247
	v_mul_f32_e32 v246, 0x42000000, v58
	v_mul_f32_e32 v247, 0x42000000, v62
	v_cvt_pk_fp8_f32 v251, v246, v247 op_sel:[0,0,1]
	s_nop 0
	global_store_dwordx4 v245, v[248:251], s[100:101]
	v_mul_f32_e32 v246, 0x42000000, v3
	v_mul_f32_e32 v247, 0x42000000, v7
	v_mov_b32_e32 v248, 0
	v_cvt_pk_fp8_f32 v248, v246, v247
	v_mul_f32_e32 v246, 0x42000000, v11
	v_mul_f32_e32 v247, 0x42000000, v15
	v_cvt_pk_fp8_f32 v248, v246, v247 op_sel:[0,0,1]
	v_mul_f32_e32 v246, 0x42000000, v19
	v_mul_f32_e32 v247, 0x42000000, v23
	v_mov_b32_e32 v249, 0
	v_cvt_pk_fp8_f32 v249, v246, v247
	v_mul_f32_e32 v246, 0x42000000, v27
	v_mul_f32_e32 v247, 0x42000000, v31
	v_cvt_pk_fp8_f32 v249, v246, v247 op_sel:[0,0,1]
	v_mul_f32_e32 v246, 0x42000000, v35
	v_mul_f32_e32 v247, 0x42000000, v39
	v_mov_b32_e32 v250, 0
	v_cvt_pk_fp8_f32 v250, v246, v247
	v_mul_f32_e32 v246, 0x42000000, v43
	v_mul_f32_e32 v247, 0x42000000, v47
	v_cvt_pk_fp8_f32 v250, v246, v247 op_sel:[0,0,1]
	v_mul_f32_e32 v246, 0x42000000, v51
	v_mul_f32_e32 v247, 0x42000000, v55
	v_mov_b32_e32 v251, 0
	v_cvt_pk_fp8_f32 v251, v246, v247
	v_mul_f32_e32 v246, 0x42000000, v59
	v_mul_f32_e32 v247, 0x42000000, v63
	v_cvt_pk_fp8_f32 v251, v246, v247 op_sel:[0,0,1]
	s_nop 0
	global_store_dwordx4 v245, v[248:251], s[100:101] offset:2048
	s_add_i32 s98, s98, 0x800
	s_mov_b32 s99, 0

.LBB0_1184:
.Lp9_cl_loop:
	s_cmp_lt_u32 s98, 0x18000
	s_cbranch_scc0 .Lp9_cl_done
	s_mov_b32 s99, s98
	v_mbcnt_lo_u32_b32 v244, -1, 0
	v_mbcnt_hi_u32_b32 v244, -1, v244
	s_sub_i32 s100, s99, 0x10000
	s_lshr_b32 s100, s100, 10
	s_lshl_b32 s100, s100, 24
	s_bfe_u32 s101, s99, 0x40006
	s_lshl_b32 s101, s101, 20
	s_add_i32 s100, s100, s101
	s_and_b32 s101, s99, 63
	s_lshl_b32 s101, s101, 7
	s_add_i32 s100, s100, s101
	v_lshrrev_b32_e32 v245, 3, v244
	v_and_b32_e32 v246, 7, v244
	v_lshlrev_b32_e32 v245, 17, v245
	v_lshl_or_b32 v245, v246, 4, v245
	v_add_u32_e32 v245, s100, v245
	v_readlane_b32 s100, v254, 42
	v_readlane_b32 s101, v254, 43
	s_nop 4
	global_load_dwordx4 v[0:3], v245, s[100:101] nt
	v_add_u32_e32 v245, 0x2000, v245
	global_load_dwordx4 v[4:7], v245, s[100:101] nt
	v_add_u32_e32 v245, 0x2000, v245
	global_load_dwordx4 v[8:11], v245, s[100:101] nt
	v_add_u32_e32 v245, 0x2000, v245
	global_load_dwordx4 v[12:15], v245, s[100:101] nt
	v_add_u32_e32 v245, 0x2000, v245
	global_load_dwordx4 v[16:19], v245, s[100:101] nt
	v_add_u32_e32 v245, 0x2000, v245
	global_load_dwordx4 v[20:23], v245, s[100:101] nt
	v_add_u32_e32 v245, 0x2000, v245
	global_load_dwordx4 v[24:27], v245, s[100:101] nt
	v_add_u32_e32 v245, 0x2000, v245
	global_load_dwordx4 v[28:31], v245, s[100:101] nt
	v_add_u32_e32 v245, 0x2000, v245
	global_load_dwordx4 v[32:35], v245, s[100:101] nt
	v_add_u32_e32 v245, 0x2000, v245
	global_load_dwordx4 v[36:39], v245, s[100:101] nt
	v_add_u32_e32 v245, 0x2000, v245
	global_load_dwordx4 v[40:43], v245, s[100:101] nt
	v_add_u32_e32 v245, 0x2000, v245
	global_load_dwordx4 v[44:47], v245, s[100:101] nt
	v_add_u32_e32 v245, 0x2000, v245
	global_load_dwordx4 v[48:51], v245, s[100:101] nt
	v_add_u32_e32 v245, 0x2000, v245
	global_load_dwordx4 v[52:55], v245, s[100:101] nt
	v_add_u32_e32 v245, 0x2000, v245
	global_load_dwordx4 v[56:59], v245, s[100:101] nt
	v_add_u32_e32 v245, 0x2000, v245
	global_load_dwordx4 v[60:63], v245, s[100:101] nt
	s_sub_i32 s100, s99, 0x10000
	s_lshr_b32 s100, s100, 10
	s_lshl_b32 s100, s100, 22
	s_and_b32 s101, s99, 63
	s_lshl_b32 s101, s101, 16
	s_add_i32 s100, s100, s101
	s_bfe_u32 s101, s99, 0x40006
	s_lshl_b32 s101, s101, 7
	s_add_i32 s100, s100, s101
	v_mbcnt_lo_u32_b32 v244, -1, 0
	v_mbcnt_hi_u32_b32 v244, -1, v244
	v_lshrrev_b32_e32 v245, 3, v244
	v_and_b32_e32 v246, 7, v244
	v_lshlrev_b32_e32 v245, 4, v245
	v_lshl_or_b32 v245, v246, 13, v245
	v_add_u32_e32 v245, s100, v245
	v_readlane_b32 s100, v254, 48
	v_readlane_b32 s101, v254, 49
	s_add_u32 s100, s100, 0x14d59400
	s_addc_u32 s101, s101, 0
	s_waitcnt vmcnt(0)
	v_mul_f32_e32 v246, 0x42000000, v0
	v_mul_f32_e32 v247, 0x42000000, v4
	v_mov_b32_e32 v248, 0
	v_cvt_pk_fp8_f32 v248, v246, v247
	v_mul_f32_e32 v246, 0x42000000, v8
	v_mul_f32_e32 v247, 0x42000000, v12
	v_cvt_pk_fp8_f32 v248, v246, v247 op_sel:[0,0,1]
	v_mul_f32_e32 v246, 0x42000000, v16
	v_mul_f32_e32 v247, 0x42000000, v20
	v_mov_b32_e32 v249, 0
	v_cvt_pk_fp8_f32 v249, v246, v247
	v_mul_f32_e32 v246, 0x42000000, v24
	v_mul_f32_e32 v247, 0x42000000, v28
	v_cvt_pk_fp8_f32 v249, v246, v247 op_sel:[0,0,1]
	v_mul_f32_e32 v246, 0x42000000, v32
	v_mul_f32_e32 v247, 0x42000000, v36
	v_mov_b32_e32 v250, 0
	v_cvt_pk_fp8_f32 v250, v246, v247
	v_mul_f32_e32 v246, 0x42000000, v40
	v_mul_f32_e32 v247, 0x42000000, v44
	v_cvt_pk_fp8_f32 v250, v246, v247 op_sel:[0,0,1]
	v_mul_f32_e32 v246, 0x42000000, v48
	v_mul_f32_e32 v247, 0x42000000, v52
	v_mov_b32_e32 v251, 0
	v_cvt_pk_fp8_f32 v251, v246, v247
	v_mul_f32_e32 v246, 0x42000000, v56
	v_mul_f32_e32 v247, 0x42000000, v60
	v_cvt_pk_fp8_f32 v251, v246, v247 op_sel:[0,0,1]
	s_nop 0
	global_store_dwordx4 v245, v[248:251], s[100:101]
	v_mul_f32_e32 v246, 0x42000000, v1
	v_mul_f32_e32 v247, 0x42000000, v5
	v_mov_b32_e32 v248, 0
	v_cvt_pk_fp8_f32 v248, v246, v247
	v_mul_f32_e32 v246, 0x42000000, v9
	v_mul_f32_e32 v247, 0x42000000, v13
	v_cvt_pk_fp8_f32 v248, v246, v247 op_sel:[0,0,1]
	v_mul_f32_e32 v246, 0x42000000, v17
	v_mul_f32_e32 v247, 0x42000000, v21
	v_mov_b32_e32 v249, 0
	v_cvt_pk_fp8_f32 v249, v246, v247
	v_mul_f32_e32 v246, 0x42000000, v25
	v_mul_f32_e32 v247, 0x42000000, v29
	v_cvt_pk_fp8_f32 v249, v246, v247 op_sel:[0,0,1]
	v_mul_f32_e32 v246, 0x42000000, v33
	v_mul_f32_e32 v247, 0x42000000, v37
	v_mov_b32_e32 v250, 0
	v_cvt_pk_fp8_f32 v250, v246, v247
	v_mul_f32_e32 v246, 0x42000000, v41
	v_mul_f32_e32 v247, 0x42000000, v45
	v_cvt_pk_fp8_f32 v250, v246, v247 op_sel:[0,0,1]
	v_mul_f32_e32 v246, 0x42000000, v49
	v_mul_f32_e32 v247, 0x42000000, v53
	v_mov_b32_e32 v251, 0
	v_cvt_pk_fp8_f32 v251, v246, v247
	v_mul_f32_e32 v246, 0x42000000, v57
	v_mul_f32_e32 v247, 0x42000000, v61
	v_cvt_pk_fp8_f32 v251, v246, v247 op_sel:[0,0,1]
	s_nop 0
	global_store_dwordx4 v245, v[248:251], s[100:101] offset:2048
	v_add_u32_e32 v245, 0x1000, v245
	v_mul_f32_e32 v246, 0x42000000, v2
	v_mul_f32_e32 v247, 0x42000000, v6
	v_mov_b32_e32 v248, 0
	v_cvt_pk_fp8_f32 v248, v246, v247
	v_mul_f32_e32 v246, 0x42000000, v10
	v_mul_f32_e32 v247, 0x42000000, v14
	v_cvt_pk_fp8_f32 v248, v246, v247 op_sel:[0,0,1]
	v_mul_f32_e32 v246, 0x42000000, v18
	v_mul_f32_e32 v247, 0x42000000, v22
	v_mov_b32_e32 v249, 0
	v_cvt_pk_fp8_f32 v249, v246, v247
	v_mul_f32_e32 v246, 0x42000000, v26
	v_mul_f32_e32 v247, 0x42000000, v30
	v_cvt_pk_fp8_f32 v249, v246, v247 op_sel:[0,0,1]
	v_mul_f32_e32 v246, 0x42000000, v34
	v_mul_f32_e32 v247, 0x42000000, v38
	v_mov_b32_e32 v250, 0
	v_cvt_pk_fp8_f32 v250, v246, v247
	v_mul_f32_e32 v246, 0x42000000, v42
	v_mul_f32_e32 v247, 0x42000000, v46
	v_cvt_pk_fp8_f32 v250, v246, v247 op_sel:[0,0,1]
	v_mul_f32_e32 v246, 0x42000000, v50
	v_mul_f32_e32 v247, 0x42000000, v54
	v_mov_b32_e32 v251, 0
	v_cvt_pk_fp8_f32 v251, v246, v247
	v_mul_f32_e32 v246, 0x42000000, v58
	v_mul_f32_e32 v247, 0x42000000, v62
	v_cvt_pk_fp8_f32 v251, v246, v247 op_sel:[0,0,1]
	s_nop 0
	global_store_dwordx4 v245, v[248:251], s[100:101]
	v_mul_f32_e32 v246, 0x42000000, v3
	v_mul_f32_e32 v247, 0x42000000, v7
	v_mov_b32_e32 v248, 0
	v_cvt_pk_fp8_f32 v248, v246, v247
	v_mul_f32_e32 v246, 0x42000000, v11
	v_mul_f32_e32 v247, 0x42000000, v15
	v_cvt_pk_fp8_f32 v248, v246, v247 op_sel:[0,0,1]
	v_mul_f32_e32 v246, 0x42000000, v19
	v_mul_f32_e32 v247, 0x42000000, v23
	v_mov_b32_e32 v249, 0
	v_cvt_pk_fp8_f32 v249, v246, v247
	v_mul_f32_e32 v246, 0x42000000, v27
	v_mul_f32_e32 v247, 0x42000000, v31
	v_cvt_pk_fp8_f32 v249, v246, v247 op_sel:[0,0,1]
	v_mul_f32_e32 v246, 0x42000000, v35
	v_mul_f32_e32 v247, 0x42000000, v39
	v_mov_b32_e32 v250, 0
	v_cvt_pk_fp8_f32 v250, v246, v247
	v_mul_f32_e32 v246, 0x42000000, v43
	v_mul_f32_e32 v247, 0x42000000, v47
	v_cvt_pk_fp8_f32 v250, v246, v247 op_sel:[0,0,1]
	v_mul_f32_e32 v246, 0x42000000, v51
	v_mul_f32_e32 v247, 0x42000000, v55
	v_mov_b32_e32 v251, 0
	v_cvt_pk_fp8_f32 v251, v246, v247
	v_mul_f32_e32 v246, 0x42000000, v59
	v_mul_f32_e32 v247, 0x42000000, v63
	v_cvt_pk_fp8_f32 v251, v246, v247 op_sel:[0,0,1]
	s_nop 0
	global_store_dwordx4 v245, v[248:251], s[100:101] offset:2048
	s_add_i32 s98, s98, 0x800
	s_mov_b32 s99, 0
	s_branch .Lp9_cl_loop

; __global__ void __launch_bounds__(NTHREADS, 2) fwd(Args args) {
;     extern __shared__ __attribute__((aligned(16))) unsigned char lds_raw[];
	.amdhsa_kernel _Z3fwd4Args
		.amdhsa_group_segment_fixed_size 0
		.amdhsa_private_segment_fixed_size 0
		.amdhsa_kernarg_size 456
		.amdhsa_user_sgpr_count 2
		.amdhsa_user_sgpr_dispatch_ptr 0
		.amdhsa_user_sgpr_queue_ptr 0
		.amdhsa_user_sgpr_kernarg_segment_ptr 1
		.amdhsa_user_sgpr_dispatch_id 0
		.amdhsa_user_sgpr_kernarg_preload_length 0
		.amdhsa_user_sgpr_kernarg_preload_offset 0
		.amdhsa_user_sgpr_private_segment_size 0
		.amdhsa_uses_dynamic_stack 0
		.amdhsa_enable_private_segment 0
		.amdhsa_system_sgpr_workgroup_id_x 1
		.amdhsa_system_sgpr_workgroup_id_y 0
		.amdhsa_system_sgpr_workgroup_id_z 0
		.amdhsa_system_sgpr_workgroup_info 0
		.amdhsa_system_vgpr_workitem_id 0
		.amdhsa_next_free_vgpr 256
		.amdhsa_next_free_sgpr 102
		.amdhsa_accum_offset 256
		.amdhsa_reserve_vcc 1
		.amdhsa_float_round_mode_32 0
		.amdhsa_float_round_mode_16_64 0
		.amdhsa_float_denorm_mode_32 3
		.amdhsa_float_denorm_mode_16_64 3
		.amdhsa_dx10_clamp 1
		.amdhsa_ieee_mode 1
		.amdhsa_fp16_overflow 0
		.amdhsa_tg_split 0
		.amdhsa_exception_fp_ieee_invalid_op 0
		.amdhsa_exception_fp_denorm_src 0
		.amdhsa_exception_fp_ieee_div_zero 0
		.amdhsa_exception_fp_ieee_overflow 0
		.amdhsa_exception_fp_ieee_underflow 0
		.amdhsa_exception_fp_ieee_inexact 0
		.amdhsa_exception_int_div_zero 0
	.end_amdhsa_kernel

; __global__ void __launch_bounds__(NTHREADS, 2) fwd(Args args) {
;     extern __shared__ __attribute__((aligned(16))) unsigned char lds_raw[];
amdhsa.kernels:
  - .agpr_count:     0
    .args:
      - .offset:         0
        .size:           200
        .value_kind:     by_value
      - .offset:         200
        .size:           4
        .value_kind:     hidden_block_count_x
      - .offset:         204
        .size:           4
        .value_kind:     hidden_block_count_y
      - .offset:         208
        .size:           4
        .value_kind:     hidden_block_count_z
      - .offset:         212
        .size:           2
        .value_kind:     hidden_group_size_x
      - .offset:         214
        .size:           2
        .value_kind:     hidden_group_size_y
      - .offset:         216
        .size:           2
        .value_kind:     hidden_group_size_z
      - .offset:         218
        .size:           2
        .value_kind:     hidden_remainder_x
      - .offset:         220
        .size:           2
        .value_kind:     hidden_remainder_y
      - .offset:         222
        .size:           2
        .value_kind:     hidden_remainder_z
      - .offset:         240
        .size:           8
        .value_kind:     hidden_global_offset_x
      - .offset:         248
        .size:           8
        .value_kind:     hidden_global_offset_y
      - .offset:         256
        .size:           8
        .value_kind:     hidden_global_offset_z
      - .offset:         264
        .size:           2
        .value_kind:     hidden_grid_dims
      - .offset:         320
        .size:           4
        .value_kind:     hidden_dynamic_lds_size
    .group_segment_fixed_size: 0
    .kernarg_segment_align: 8
    .kernarg_segment_size: 456
    .language:       OpenCL C
    .language_version:
      - 2
      - 0
    .max_flat_workgroup_size: 512
    .name:           _Z3fwd4Args
    .private_segment_fixed_size: 0
    .sgpr_count:     108
    .sgpr_spill_count: 115
    .symbol:         _Z3fwd4Args.kd
    .uniform_work_group_size: 1
    .uses_dynamic_stack: false
    .vgpr_count:     256
    .vgpr_spill_count: 0
    .wavefront_size: 64
